# plus: mix_unit up-projection weight loads hoisted, router pass-1 loads batched, HGRN A-block loop LDS reads pipelined
# speedup vs baseline: 1.0356x; 1.0115x over previous
.LBB0_400:
	s_or_b64 exec, exec, s[0:1]
	s_ashr_i32 s0, s55, 31
	s_lshr_b32 s0, s0, 24
	s_add_i32 s0, s55, s0
	v_and_b32_e32 v91, 15, v1
	v_ashrrev_i32_e32 v88, 4, v1
	s_ashr_i32 s2, s0, 8
	v_lshlrev_b32_e32 v82, 3, v88
	v_xor_b32_e32 v98, 16, v228
	v_xor_b32_e32 v97, 32, v228
	v_lshlrev_b32_e32 v78, 2, v88
	v_or_b32_e32 v80, s90, v91
	s_mov_b64 s[18:19], -1
	s_cmp_gt_i32 s91, 3
	v_lshlrev_b32_e32 v92, 4, v88
	v_ashrrev_i32_e32 v83, 31, v82
	v_cmp_lt_i32_e64 s[0:1], v98, v96
	v_cmp_lt_i32_e32 vcc, v97, v96
	v_ashrrev_i32_e32 v79, 31, v78
	v_ashrrev_i32_e32 v81, 31, v80
	s_waitcnt lgkmcnt(0)
	s_barrier
	s_cbranch_scc0 .LBB0_402
	s_add_i32 s3, s91, -4
	s_lshl_b32 s80, s3, 7
	s_lshl_b64 s[18:19], s[80:81], 8
	s_add_u32 s18, s28, s18
	s_addc_u32 s19, s29, s19
	v_lshlrev_b32_e32 v114, 8, v91
	v_lshl_add_u64 v[2:3], s[18:19], 0, v[114:115]
	v_lshl_add_u64 v[18:19], v[82:83], 1, v[2:3]
	s_movk_i32 s17, 0x4000
	v_add_co_u32_e64 v20, s[38:39], s17, v18
	s_movk_i32 s17, 0x5000
	s_nop 0
	v_addc_co_u32_e64 v21, s[38:39], 0, v19, s[38:39]
	v_add_co_u32_e64 v22, s[38:39], s17, v18
	s_movk_i32 s17, 0x1000
	s_nop 0
	v_addc_co_u32_e64 v23, s[38:39], 0, v19, s[38:39]
	v_add_co_u32_e64 v24, s[38:39], s17, v18
	s_movk_i32 s17, 0x2000
	s_nop 0
	v_addc_co_u32_e64 v25, s[38:39], 0, v19, s[38:39]
	v_add_co_u32_e64 v60, s[38:39], s17, v18
	v_mul_u32_u24_e32 v4, 0x88, v91
	s_nop 0
	v_addc_co_u32_e64 v61, s[38:39], 0, v19, s[38:39]
	s_movk_i32 s17, 0x6000
	v_lshlrev_b32_e32 v4, 1, v4
	v_add_co_u32_e64 v58, s[38:39], s17, v18
	v_add3_u32 v89, 0, v92, v4
	s_nop 0
	v_addc_co_u32_e64 v59, s[38:39], 0, v19, s[38:39]
	s_movk_i32 s17, 0x7000
	ds_read_b128 v[26:29], v89 offset:12800
	ds_read_b128 v[30:33], v89 offset:17152
	global_load_dwordx4 v[6:9], v[18:19], off
	global_load_dwordx4 v[14:17], v[22:23], off offset:-4096
	global_load_dwordx4 v[34:37], v[60:61], off offset:-4096
	global_load_dwordx4 v[38:41], v[22:23], off
	global_load_dwordx4 v[50:53], v[60:61], off
	v_add_co_u32_e64 v84, s[38:39], s17, v18
	s_movk_i32 s17, 0x3000
	s_nop 0
	v_addc_co_u32_e64 v85, s[38:39], 0, v19, s[38:39]
	v_add_co_u32_e64 v86, s[38:39], s17, v18
	global_load_dwordx4 v[54:57], v[84:85], off offset:-4096
	s_nop 0
	v_addc_co_u32_e64 v87, s[38:39], 0, v19, s[38:39]
	global_load_dwordx4 v[70:73], v[86:87], off
	global_load_dwordx4 v[74:77], v[84:85], off
	global_load_dwordx4 v[140:143], v[18:19], off offset:64
	global_load_dwordx4 v[144:147], v[20:21], off offset:64
	global_load_dwordx4 v[148:151], v[24:25], off offset:64
	global_load_dwordx4 v[152:155], v[22:23], off offset:64
	global_load_dwordx4 v[156:159], v[60:61], off offset:64
	global_load_dwordx4 v[160:163], v[58:59], off offset:64
	global_load_dwordx4 v[164:167], v[86:87], off offset:64
	global_load_dwordx4 v[168:171], v[84:85], off offset:64
	global_load_dwordx4 v[172:175], v[18:19], off offset:128
	global_load_dwordx4 v[176:179], v[20:21], off offset:128
	global_load_dwordx4 v[180:183], v[24:25], off offset:128
	global_load_dwordx4 v[184:187], v[22:23], off offset:128
	global_load_dwordx4 v[188:191], v[60:61], off offset:128
	global_load_dwordx4 v[192:195], v[58:59], off offset:128
	global_load_dwordx4 v[196:199], v[86:87], off offset:128
	global_load_dwordx4 v[200:203], v[84:85], off offset:128
	global_load_dwordx4 v[204:207], v[18:19], off offset:192
	global_load_dwordx4 v[208:211], v[20:21], off offset:192
	global_load_dwordx4 v[212:215], v[24:25], off offset:192
	global_load_dwordx4 v[216:219], v[22:23], off offset:192
	global_load_dwordx4 v[220:223], v[60:61], off offset:192
	global_load_dwordx4 v[234:237], v[58:59], off offset:192
	global_load_dwordx4 v[238:241], v[86:87], off offset:192
	global_load_dwordx4 v[242:245], v[84:85], off offset:192
	s_ashr_i32 s17, s16, 31
	v_readlane_b32 s36, v253, 11
	v_readlane_b32 s37, v253, 12
	v_lshlrev_b32_e32 v114, 14, v91
	v_or_b32_e32 v99, 16, v91
	s_waitcnt vmcnt(31) lgkmcnt(1)
	v_mfma_f32_16x16x32_bf16 v[2:5], v[6:9], v[26:29], 0
	s_waitcnt lgkmcnt(0)
	v_mfma_f32_16x16x32_bf16 v[6:9], v[6:9], v[30:33], 0
	s_waitcnt vmcnt(30)
	v_mfma_f32_16x16x32_bf16 v[10:13], v[26:29], v[14:17], 0
	v_mfma_f32_16x16x32_bf16 v[14:17], v[30:33], v[14:17], 0
	s_waitcnt vmcnt(29)
	v_mfma_f32_16x16x32_bf16 v[42:45], v[34:37], v[26:29], 0
	v_mfma_f32_16x16x32_bf16 v[34:37], v[34:37], v[30:33], 0
	s_waitcnt vmcnt(28)
	v_mfma_f32_16x16x32_bf16 v[46:49], v[26:29], v[38:41], 0
	v_mfma_f32_16x16x32_bf16 v[38:41], v[30:33], v[38:41], 0
	s_waitcnt vmcnt(27)
	v_mfma_f32_16x16x32_bf16 v[62:65], v[50:53], v[26:29], 0
	v_mfma_f32_16x16x32_bf16 v[50:53], v[50:53], v[30:33], 0
	s_waitcnt vmcnt(26)
	v_mfma_f32_16x16x32_bf16 v[66:69], v[26:29], v[54:57], 0
	v_mfma_f32_16x16x32_bf16 v[54:57], v[30:33], v[54:57], 0
	s_waitcnt vmcnt(25)
	v_mfma_f32_16x16x32_bf16 v[100:103], v[70:73], v[26:29], 0
	v_mfma_f32_16x16x32_bf16 v[70:73], v[70:73], v[30:33], 0
	s_waitcnt vmcnt(24)
	v_mfma_f32_16x16x32_bf16 v[26:29], v[26:29], v[74:77], 0
	v_mfma_f32_16x16x32_bf16 v[30:33], v[30:33], v[74:77], 0
	ds_read_b128 v[74:77], v89 offset:12864
	ds_read_b128 v[104:107], v89 offset:17216
	s_waitcnt vmcnt(23) lgkmcnt(1)
	v_mfma_f32_16x16x32_bf16 v[2:5], v[140:143], v[74:77], v[2:5]
	s_waitcnt lgkmcnt(0)
	v_mfma_f32_16x16x32_bf16 v[6:9], v[140:143], v[104:107], v[6:9]
	s_waitcnt vmcnt(22)
	v_mfma_f32_16x16x32_bf16 v[10:13], v[74:77], v[144:147], v[10:13]
	v_mfma_f32_16x16x32_bf16 v[14:17], v[104:107], v[144:147], v[14:17]
	s_waitcnt vmcnt(21)
	v_mfma_f32_16x16x32_bf16 v[42:45], v[148:151], v[74:77], v[42:45]
	v_mfma_f32_16x16x32_bf16 v[34:37], v[148:151], v[104:107], v[34:37]
	s_waitcnt vmcnt(20)
	v_mfma_f32_16x16x32_bf16 v[46:49], v[74:77], v[152:155], v[46:49]
	v_mfma_f32_16x16x32_bf16 v[38:41], v[104:107], v[152:155], v[38:41]
	s_waitcnt vmcnt(19)
	v_mfma_f32_16x16x32_bf16 v[62:65], v[156:159], v[74:77], v[62:65]
	v_mfma_f32_16x16x32_bf16 v[50:53], v[156:159], v[104:107], v[50:53]
	s_waitcnt vmcnt(18)
	v_mfma_f32_16x16x32_bf16 v[66:69], v[74:77], v[160:163], v[66:69]
	v_mfma_f32_16x16x32_bf16 v[54:57], v[104:107], v[160:163], v[54:57]
	s_waitcnt vmcnt(17)
	v_mfma_f32_16x16x32_bf16 v[100:103], v[164:167], v[74:77], v[100:103]
	v_mfma_f32_16x16x32_bf16 v[70:73], v[164:167], v[104:107], v[70:73]
	s_waitcnt vmcnt(16)
	v_mfma_f32_16x16x32_bf16 v[74:77], v[74:77], v[168:171], v[26:29]
	v_mfma_f32_16x16x32_bf16 v[104:107], v[104:107], v[168:171], v[30:33]
	ds_read_b128 v[108:111], v89 offset:12928
	ds_read_b128 v[116:119], v89 offset:17280
	s_waitcnt vmcnt(14) lgkmcnt(1)
	v_mfma_f32_16x16x32_bf16 v[120:123], v[108:111], v[176:179], v[10:13]
	s_waitcnt lgkmcnt(0)
	v_mfma_f32_16x16x32_bf16 v[124:127], v[116:119], v[176:179], v[14:17]
	s_nop 0
	s_nop 0
	s_waitcnt vmcnt(12)
	v_mfma_f32_16x16x32_bf16 v[46:49], v[108:111], v[184:187], v[46:49]
	v_mfma_f32_16x16x32_bf16 v[136:139], v[116:119], v[184:187], v[38:41]
	v_mfma_f32_16x16x32_bf16 v[128:131], v[180:183], v[108:111], v[42:45]
	v_mfma_f32_16x16x32_bf16 v[132:135], v[180:183], v[116:119], v[34:37]
	s_waitcnt vmcnt(11)
	v_mfma_f32_16x16x32_bf16 v[10:13], v[188:191], v[108:111], v[62:65]
	s_waitcnt vmcnt(10)
	v_mfma_f32_16x16x32_bf16 v[42:45], v[108:111], v[192:195], v[66:69]
	v_mfma_f32_16x16x32_bf16 v[62:65], v[116:119], v[192:195], v[54:57]
	v_mfma_f32_16x16x32_bf16 v[2:5], v[172:175], v[108:111], v[2:5]
	v_mfma_f32_16x16x32_bf16 v[6:9], v[172:175], v[116:119], v[6:9]
	v_mfma_f32_16x16x32_bf16 v[26:29], v[188:191], v[116:119], v[50:53]
	s_waitcnt vmcnt(9)
	v_mfma_f32_16x16x32_bf16 v[14:17], v[196:199], v[108:111], v[100:103]
	v_mfma_f32_16x16x32_bf16 v[30:33], v[196:199], v[116:119], v[70:73]
	s_waitcnt vmcnt(8)
	v_mfma_f32_16x16x32_bf16 v[38:41], v[108:111], v[200:203], v[74:77]
	s_nop 0
	ds_read_b128 v[70:73], v89 offset:12992
	s_nop 0
	ds_read_b128 v[74:77], v89 offset:17344
	v_mfma_f32_16x16x32_bf16 v[66:69], v[116:119], v[200:203], v[104:107]
	s_waitcnt vmcnt(7) lgkmcnt(0)
	v_mfma_f32_16x16x32_bf16 v[18:21], v[204:207], v[74:77], v[6:9]
	s_nop 2
	v_mfma_f32_16x16x32_bf16 v[50:53], v[204:207], v[70:73], v[2:5]
	s_waitcnt vmcnt(6)
	v_mfma_f32_16x16x32_bf16 v[34:37], v[70:73], v[208:211], v[120:123]
	v_mfma_f32_16x16x32_bf16 v[2:5], v[74:77], v[208:211], v[124:127]
	s_waitcnt vmcnt(5)
	v_mfma_f32_16x16x32_bf16 v[54:57], v[212:215], v[70:73], v[128:131]
	s_nop 4
	v_cvt_pk_bf16_f32 v34, v34, v35
	v_cvt_pk_bf16_f32 v35, v36, v37
	v_cvt_pk_bf16_f32 v2, v2, v3
	v_mfma_f32_16x16x32_bf16 v[22:25], v[212:215], v[74:77], v[132:135]
	v_cvt_pk_bf16_f32 v3, v4, v5
	s_waitcnt vmcnt(4)
	v_mfma_f32_16x16x32_bf16 v[46:49], v[70:73], v[216:219], v[46:49]
	v_mfma_f32_16x16x32_bf16 v[6:9], v[74:77], v[216:219], v[136:139]
	s_nop 4
	v_cvt_pk_bf16_f32 v46, v46, v47
	v_cvt_pk_bf16_f32 v47, v48, v49
	s_waitcnt vmcnt(3)
	v_mfma_f32_16x16x32_bf16 v[58:61], v[220:223], v[70:73], v[10:13]
	v_mfma_f32_16x16x32_bf16 v[26:29], v[220:223], v[74:77], v[26:29]
	s_nop 0
	s_waitcnt vmcnt(2)
	v_mfma_f32_16x16x32_bf16 v[10:13], v[74:77], v[234:237], v[62:65]
	s_waitcnt vmcnt(1)
	v_mfma_f32_16x16x32_bf16 v[62:65], v[238:241], v[70:73], v[14:17]
	v_mfma_f32_16x16x32_bf16 v[30:33], v[238:241], v[74:77], v[30:33]
	v_lshl_add_u32 v103, v91, 7, 0
	v_lshlrev_b32_e32 v102, 5, v88
	s_waitcnt vmcnt(0)
	v_mfma_f32_16x16x32_bf16 v[14:17], v[74:77], v[242:245], v[66:69]
	v_mul_f32_e32 v76, v51, v51
	v_fmac_f32_e32 v76, v50, v50
	v_fmac_f32_e32 v76, v52, v52
	v_fmac_f32_e32 v76, v53, v53
	v_fmac_f32_e32 v76, v54, v54
	v_fmac_f32_e32 v76, v55, v55
	v_fmac_f32_e32 v76, v56, v56
	v_fmac_f32_e32 v76, v57, v57
	v_fmac_f32_e32 v76, v58, v58
	v_fmac_f32_e32 v76, v59, v59
	v_fmac_f32_e32 v76, v60, v60
	v_mfma_f32_16x16x32_bf16 v[42:45], v[70:73], v[234:237], v[42:45]
	v_fmac_f32_e32 v76, v61, v61
	v_add_u32_e32 v104, v103, v102
	v_fmac_f32_e32 v76, v62, v62
	v_mfma_f32_16x16x32_bf16 v[38:41], v[70:73], v[242:245], v[38:41]
	ds_read_b128 v[86:89], v104 offset:21504
	ds_read_b128 v[106:109], v104 offset:21520
	v_fmac_f32_e32 v76, v63, v63
	v_fmac_f32_e32 v76, v64, v64
	v_fmac_f32_e32 v76, v65, v65
	s_waitcnt lgkmcnt(1)
	v_fmac_f32_e32 v76, v86, v86
	v_fmac_f32_e32 v76, v87, v87
	v_pk_mul_f32 v[68:69], v[88:89], v[88:89]
	v_cndmask_b32_e64 v66, v228, v98, s[0:1]
	v_add_f32_e32 v68, v68, v76
	v_add_f32_e32 v76, v69, v68
	s_waitcnt lgkmcnt(0)
	v_pk_mul_f32 v[68:69], v[106:107], v[106:107]
	v_lshlrev_b32_e32 v100, 2, v66
	v_add_f32_e32 v68, v68, v76
	v_add_f32_e32 v76, v69, v68
	v_pk_mul_f32 v[68:69], v[108:109], v[108:109]
	s_lshl_b32 s0, s2, 2
	v_add_f32_e32 v68, v68, v76
	v_add_f32_e32 v68, v69, v68
	ds_bpermute_b32 v69, v100, v68
	s_add_i32 s0, s3, s0
	s_ashr_i32 s1, s0, 31
	v_cndmask_b32_e32 v66, v228, v97, vcc
	s_lshl_b64 s[18:19], s[0:1], 13
	v_lshlrev_b32_e32 v101, 2, v66
	s_add_u32 s18, s18, s16
	s_waitcnt lgkmcnt(0)
	v_add_f32_e32 v68, v68, v69
	s_addc_u32 s3, s19, s17
	s_lshl_b64 s[0:1], s[0:1], 20
	v_readlane_b32 s19, v253, 17
	ds_bpermute_b32 v69, v101, v68
	s_add_u32 s19, s19, s0
	v_readlane_b32 s0, v253, 18
	s_addc_u32 s38, s0, s1
	s_lshl_b64 s[0:1], s[16:17], 1
	s_add_u32 s0, s19, s0
	s_addc_u32 s1, s38, s1
	v_lshlrev_b64 v[84:85], 1, v[78:79]
	v_lshl_add_u64 v[70:71], s[0:1], 0, v[84:85]
	s_waitcnt lgkmcnt(0)
	v_add_f32_e32 v68, v68, v69
	v_readlane_b32 s0, v253, 15
	v_fmamk_f32 v68, v68, 0x3c2aaaab, v225
	v_readlane_b32 s1, v253, 16
	v_lshlrev_b64 v[66:67], 2, v[78:79]
	v_rsq_f32_e32 v90, v68
	v_or_b32_e32 v68, s18, v91
	v_mov_b64_e32 v[86:87], s[0:1]
	v_lshl_add_u64 v[72:73], s[36:37], 0, v[66:67]
	v_readlane_b32 s36, v253, 13
	v_mad_u64_u32 v[68:69], s[0:1], v68, s8, v[86:87]
	v_mov_b32_e32 v108, 0xc0
	v_readlane_b32 s37, v253, 14
	v_mad_i32_i24 v69, s3, v108, v69
	v_lshl_add_u64 v[76:77], s[22:23], 0, v[66:67]
	v_lshl_add_u64 v[74:75], s[36:37], 0, v[66:67]
	v_lshl_add_u64 v[88:89], v[68:69], 0, v[84:85]
	global_load_dwordx4 v[66:69], v[76:77], off
	v_pk_mul_f32 v[50:51], v[50:51], v[90:91] op_sel_hi:[1,0]
	v_pk_mul_f32 v[52:53], v[52:53], v[90:91] op_sel_hi:[1,0]
	v_pk_mul_f32 v[54:55], v[54:55], v[90:91] op_sel_hi:[1,0]
	v_lshl_add_u64 v[36:37], v[70:71], 0, v[114:115]
	v_cvt_pk_bf16_f32 v38, v38, v39
	v_cvt_pk_bf16_f32 v39, v40, v41
	s_waitcnt vmcnt(0)
	v_pk_mul_f32 v[50:51], v[66:67], v[50:51]
	v_pk_mul_f32 v[52:53], v[68:69], v[52:53]
	v_cvt_pk_bf16_f32 v50, v50, v51
	v_cvt_pk_bf16_f32 v51, v52, v53
	global_store_dwordx2 v[88:89], v[50:51], off
	global_load_dwordx4 v[50:53], v[76:77], off offset:64
	v_sub_u32_e32 v66, v104, v92
	ds_read_b128 v[66:69], v66 offset:21568
	s_waitcnt vmcnt(0)
	v_pk_mul_f32 v[50:51], v[50:51], v[54:55]
	v_pk_mul_f32 v[54:55], v[56:57], v[90:91] op_sel_hi:[1,0]
	v_cvt_pk_bf16_f32 v50, v50, v51
	v_pk_mul_f32 v[52:53], v[54:55], v[52:53]
	v_pk_mul_f32 v[54:55], v[58:59], v[90:91] op_sel_hi:[1,0]
	v_cvt_pk_bf16_f32 v51, v52, v53
	global_store_dwordx2 v[88:89], v[50:51], off offset:32
	global_load_dwordx4 v[50:53], v[76:77], off offset:128
	v_add_u32_e32 v58, v103, v92
	s_waitcnt vmcnt(0)
	v_pk_mul_f32 v[50:51], v[54:55], v[50:51]
	v_pk_mul_f32 v[54:55], v[60:61], v[90:91] op_sel_hi:[1,0]
	v_cvt_pk_bf16_f32 v50, v50, v51
	v_pk_mul_f32 v[52:53], v[54:55], v[52:53]
	v_pk_mul_f32 v[54:55], v[62:63], v[90:91] op_sel_hi:[1,0]
	v_cvt_pk_bf16_f32 v51, v52, v53
	global_store_dwordx2 v[88:89], v[50:51], off offset:64
	global_load_dwordx4 v[50:53], v[76:77], off offset:192
	ds_read_b128 v[58:61], v58 offset:21504
	s_waitcnt lgkmcnt(0)
	v_pk_mul_f32 v[58:59], v[90:91], v[58:59] op_sel_hi:[0,1]
	s_waitcnt vmcnt(0)
	v_pk_mul_f32 v[50:51], v[54:55], v[50:51]
	v_pk_mul_f32 v[54:55], v[64:65], v[90:91] op_sel_hi:[1,0]
	v_cvt_pk_bf16_f32 v50, v50, v51
	v_pk_mul_f32 v[52:53], v[54:55], v[52:53]
	v_lshlrev_b64 v[54:55], 6, v[80:81]
	v_cvt_pk_bf16_f32 v51, v52, v53
	global_store_dwordx2 v[88:89], v[50:51], off offset:96
	global_load_dwordx4 v[62:65], v[76:77], off offset:256
	global_load_dwordx4 v[104:107], v[76:77], off offset:320
	v_lshl_add_u64 v[50:51], v[72:73], 0, v[54:55]
	v_lshl_add_u64 v[54:55], v[74:75], 0, v[54:55]
	global_load_dwordx4 v[50:53], v[50:51], off
	s_waitcnt vmcnt(2)
	v_pk_mul_f32 v[58:59], v[58:59], v[62:63]
	global_load_dwordx4 v[54:57], v[54:55], off
	v_pk_mul_f32 v[62:63], v[90:91], v[66:67] op_sel_hi:[0,1]
	s_waitcnt vmcnt(2)
	v_pk_mul_f32 v[62:63], v[62:63], v[104:105]
	s_waitcnt vmcnt(0)
	v_pk_mul_f32 v[66:67], v[54:55], v[62:63]
	s_nop 0
	v_pk_fma_f32 v[66:67], v[50:51], v[58:59], v[66:67] neg_lo:[0,0,1] neg_hi:[0,0,1]
	v_pk_mul_f32 v[50:51], v[50:51], v[62:63]
	s_nop 0
	v_pk_fma_f32 v[50:51], v[54:55], v[58:59], v[50:51]
	v_pk_mul_f32 v[58:59], v[90:91], v[68:69] op_sel_hi:[0,1]
	v_pk_mul_f32 v[54:55], v[90:91], v[60:61] op_sel_hi:[0,1]
	v_pk_mul_f32 v[58:59], v[58:59], v[106:107]
	v_pk_mul_f32 v[54:55], v[54:55], v[64:65]
	v_pk_mul_f32 v[60:61], v[56:57], v[58:59]
	v_cvt_pk_bf16_f32 v50, v50, v51
	v_pk_fma_f32 v[60:61], v[52:53], v[54:55], v[60:61] neg_lo:[0,0,1] neg_hi:[0,0,1]
	v_pk_mul_f32 v[52:53], v[52:53], v[58:59]
	s_nop 0
	v_pk_fma_f32 v[52:53], v[56:57], v[54:55], v[52:53]
	v_cvt_pk_bf16_f32 v54, v66, v67
	v_cvt_pk_bf16_f32 v55, v60, v61
	v_cvt_pk_bf16_f32 v51, v52, v53
	global_store_dwordx2 v[88:89], v[54:55], off offset:128
	global_store_dwordx2 v[88:89], v[50:51], off offset:160
	global_store_dwordx2 v[36:37], v[34:35], off
	v_or_b32_e32 v34, 0x40000, v114
	v_mov_b32_e32 v35, v115
	v_lshl_add_u64 v[48:49], v[70:71], 0, v[34:35]
	global_store_dwordx2 v[48:49], v[46:47], off
	v_cvt_pk_bf16_f32 v46, v42, v43
	v_or_b32_e32 v42, 0x80000, v114
	v_or_b32_e32 v114, 0xc0000, v114
	v_lshl_add_u64 v[40:41], v[70:71], 0, v[114:115]
	global_store_dwordx2 v[40:41], v[38:39], off
	v_mul_f32_e32 v40, v19, v19
	v_fmac_f32_e32 v40, v18, v18
	v_fmac_f32_e32 v40, v20, v20
	v_fmac_f32_e32 v40, v21, v21
	v_fmac_f32_e32 v40, v22, v22
	v_fmac_f32_e32 v40, v23, v23
	v_fmac_f32_e32 v40, v24, v24
	v_fmac_f32_e32 v40, v25, v25
	v_fmac_f32_e32 v40, v26, v26
	v_mov_b32_e32 v43, v115
	v_fmac_f32_e32 v40, v27, v27
	v_cvt_pk_bf16_f32 v47, v44, v45
	v_lshl_add_u64 v[44:45], v[70:71], 0, v[42:43]
	v_fmac_f32_e32 v40, v28, v28
	v_lshlrev_b32_e32 v38, 7, v99
	global_store_dwordx2 v[44:45], v[46:47], off
	v_fmac_f32_e32 v40, v29, v29
	v_add3_u32 v41, 0, v38, v102
	v_fmac_f32_e32 v40, v30, v30
	ds_read_b128 v[44:47], v41 offset:21504
	ds_read_b128 v[48:51], v41 offset:21520
	v_fmac_f32_e32 v40, v31, v31
	v_fmac_f32_e32 v40, v32, v32
	v_fmac_f32_e32 v40, v33, v33
	s_waitcnt lgkmcnt(1)
	v_fmac_f32_e32 v40, v44, v44
	v_fmac_f32_e32 v40, v45, v45
	v_pk_mul_f32 v[38:39], v[46:47], v[46:47]
	global_load_dwordx4 v[44:47], v[76:77], off
	v_add_f32_e32 v38, v40, v38
	v_add_f32_e32 v40, v38, v39
	s_waitcnt lgkmcnt(0)
	v_pk_mul_f32 v[38:39], v[48:49], v[48:49]
	s_nop 0
	v_add_f32_e32 v38, v40, v38
	v_add_f32_e32 v40, v38, v39
	v_pk_mul_f32 v[38:39], v[50:51], v[50:51]
	s_nop 0
	v_add_f32_e32 v38, v40, v38
	v_add_f32_e32 v38, v38, v39
	ds_bpermute_b32 v39, v100, v38
	s_waitcnt lgkmcnt(0)
	v_add_f32_e32 v38, v38, v39
	ds_bpermute_b32 v39, v101, v38
	s_waitcnt lgkmcnt(0)
	v_add_f32_e32 v38, v38, v39
	v_fmamk_f32 v38, v38, 0x3c2aaaab, v225
	v_rsq_f32_e32 v40, v38
	v_or_b32_e32 v38, s18, v99
	v_mad_u64_u32 v[38:39], s[0:1], v38, s8, v[86:87]
	v_pk_mul_f32 v[18:19], v[18:19], v[40:41] op_sel_hi:[1,0]
	v_pk_mul_f32 v[20:21], v[20:21], v[40:41] op_sel_hi:[1,0]
	v_mad_i32_i24 v39, s3, v108, v39
	v_lshl_add_u64 v[38:39], v[38:39], 0, v[84:85]
	v_pk_mul_f32 v[22:23], v[22:23], v[40:41] op_sel_hi:[1,0]
	s_mov_b64 s[18:19], 0
	s_waitcnt vmcnt(0)
	v_pk_mul_f32 v[18:19], v[44:45], v[18:19]
	v_pk_mul_f32 v[20:21], v[46:47], v[20:21]
	v_cvt_pk_bf16_f32 v18, v18, v19
	v_cvt_pk_bf16_f32 v19, v20, v21
	global_store_dwordx2 v[38:39], v[18:19], off
	global_load_dwordx4 v[18:21], v[76:77], off offset:64
	s_waitcnt vmcnt(0)
	v_pk_mul_f32 v[18:19], v[18:19], v[22:23]
	v_pk_mul_f32 v[22:23], v[24:25], v[40:41] op_sel_hi:[1,0]
	v_cvt_pk_bf16_f32 v18, v18, v19
	v_pk_mul_f32 v[20:21], v[22:23], v[20:21]
	v_pk_mul_f32 v[22:23], v[26:27], v[40:41] op_sel_hi:[1,0]
	v_cvt_pk_bf16_f32 v19, v20, v21
	global_store_dwordx2 v[38:39], v[18:19], off offset:32
	global_load_dwordx4 v[18:21], v[76:77], off offset:128
	s_waitcnt vmcnt(0)
	v_pk_mul_f32 v[18:19], v[22:23], v[18:19]
	v_pk_mul_f32 v[22:23], v[28:29], v[40:41] op_sel_hi:[1,0]
	v_cvt_pk_bf16_f32 v18, v18, v19
	v_pk_mul_f32 v[20:21], v[22:23], v[20:21]
	v_pk_mul_f32 v[22:23], v[30:31], v[40:41] op_sel_hi:[1,0]
	v_cvt_pk_bf16_f32 v19, v20, v21
	global_store_dwordx2 v[38:39], v[18:19], off offset:64
	global_load_dwordx4 v[18:21], v[76:77], off offset:192
	s_waitcnt vmcnt(0)
	v_pk_mul_f32 v[18:19], v[22:23], v[18:19]
	v_pk_mul_f32 v[22:23], v[32:33], v[40:41] op_sel_hi:[1,0]
	v_cvt_pk_bf16_f32 v18, v18, v19
	v_pk_mul_f32 v[20:21], v[22:23], v[20:21]
	v_sub_u32_e32 v41, v41, v92
	v_cvt_pk_bf16_f32 v19, v20, v21
	global_store_dwordx2 v[38:39], v[18:19], off offset:96
	v_or_b32_e32 v18, s90, v99
	v_ashrrev_i32_e32 v19, 31, v18
	v_lshlrev_b64 v[22:23], 6, v[18:19]
	global_load_dwordx4 v[30:33], v[76:77], off offset:256
	global_load_dwordx4 v[48:51], v[76:77], off offset:320
	v_lshl_add_u64 v[18:19], v[72:73], 0, v[22:23]
	v_lshl_add_u64 v[22:23], v[74:75], 0, v[22:23]
	global_load_dwordx4 v[18:21], v[18:19], off
	ds_read_b128 v[26:29], v41 offset:21504
	ds_read_b128 v[44:47], v41 offset:21568
	global_load_dwordx4 v[22:25], v[22:23], off
	s_waitcnt lgkmcnt(1)
	v_pk_mul_f32 v[26:27], v[40:41], v[26:27] op_sel_hi:[0,1]
	s_waitcnt vmcnt(3)
	v_pk_mul_f32 v[26:27], v[26:27], v[30:31]
	s_waitcnt lgkmcnt(0)
	v_pk_mul_f32 v[30:31], v[40:41], v[44:45] op_sel_hi:[0,1]
	s_waitcnt vmcnt(2)
	v_pk_mul_f32 v[30:31], v[30:31], v[48:49]
	s_waitcnt vmcnt(0)
	v_pk_mul_f32 v[44:45], v[22:23], v[30:31]
	s_nop 0
	v_pk_fma_f32 v[44:45], v[18:19], v[26:27], v[44:45] neg_lo:[0,0,1] neg_hi:[0,0,1]
	v_pk_mul_f32 v[18:19], v[18:19], v[30:31]
	s_nop 0
	v_pk_fma_f32 v[18:19], v[22:23], v[26:27], v[18:19]
	v_pk_mul_f32 v[26:27], v[40:41], v[46:47] op_sel_hi:[0,1]
	v_pk_mul_f32 v[22:23], v[40:41], v[28:29] op_sel_hi:[0,1]
	v_pk_mul_f32 v[26:27], v[26:27], v[50:51]
	v_pk_mul_f32 v[22:23], v[22:23], v[32:33]
	v_pk_mul_f32 v[28:29], v[24:25], v[26:27]
	v_cvt_pk_bf16_f32 v18, v18, v19
	v_pk_fma_f32 v[28:29], v[20:21], v[22:23], v[28:29] neg_lo:[0,0,1] neg_hi:[0,0,1]
	v_pk_mul_f32 v[20:21], v[20:21], v[26:27]
	s_nop 0
	v_pk_fma_f32 v[20:21], v[24:25], v[22:23], v[20:21]
	v_cvt_pk_bf16_f32 v22, v44, v45
	v_cvt_pk_bf16_f32 v19, v20, v21
	v_cvt_pk_bf16_f32 v23, v28, v29
	global_store_dwordx2 v[38:39], v[18:19], off offset:160
	v_lshl_add_u64 v[18:19], v[70:71], 0, 32
	global_store_dwordx2 v[38:39], v[22:23], off offset:128
	global_store_dwordx2 v[36:37], v[2:3], off offset:32
	v_cvt_pk_bf16_f32 v2, v6, v7
	v_cvt_pk_bf16_f32 v3, v8, v9
	v_lshl_add_u64 v[4:5], v[18:19], 0, v[34:35]
	global_store_dwordx2 v[4:5], v[2:3], off
	v_cvt_pk_bf16_f32 v2, v10, v11
	v_cvt_pk_bf16_f32 v3, v12, v13
	v_lshl_add_u64 v[4:5], v[18:19], 0, v[42:43]
	global_store_dwordx2 v[4:5], v[2:3], off
	v_cvt_pk_bf16_f32 v2, v14, v15
	v_cvt_pk_bf16_f32 v3, v16, v17
	v_lshl_add_u64 v[4:5], v[18:19], 0, v[114:115]
	global_store_dwordx2 v[4:5], v[2:3], off
.LBB0_402:
	s_andn2_b64 vcc, exec, s[18:19]
	s_cbranch_vccnz .LBB0_404
	s_mul_i32 s0, s91, 0x60
	s_mul_i32 s1, s91, 0x9000
	s_mul_hi_i32 s3, s0, 0x180
	s_add_u32 s0, s26, s1
	s_addc_u32 s1, s88, s3
	v_mul_u32_u24_e32 v2, 0xc0, v91
	v_mul_u32_u24_e32 v3, 0xc8, v91
	v_lshl_add_u64 v[36:37], v[82:83], 1, s[0:1]
	v_lshlrev_b32_e32 v3, 1, v3
	v_lshlrev_b32_e32 v114, 1, v2
	v_add3_u32 v88, 0, v92, v3
	v_lshl_add_u64 v[2:3], v[36:37], 0, v[114:115]
	s_mov_b64 s[0:1], 0x1800
	v_lshl_add_u64 v[38:39], v[2:3], 0, s[0:1]
	s_movk_i32 s0, 0x1000
	v_add_co_u32_e32 v20, vcc, s0, v2
	s_movk_i32 s0, 0x3000
	s_nop 0
	v_addc_co_u32_e32 v21, vcc, 0, v3, vcc
	v_add_co_u32_e32 v64, vcc, s0, v2
	s_movk_i32 s0, 0x4000
	s_nop 0
	v_addc_co_u32_e32 v65, vcc, 0, v3, vcc
	v_add_co_u32_e32 v62, vcc, s0, v2
	s_movk_i32 s0, 0x7000
	s_nop 0
	v_addc_co_u32_e32 v63, vcc, 0, v3, vcc
	v_or_b32_e32 v114, 0x6000, v114
	v_add_co_u32_e32 v68, vcc, s0, v2
	v_lshl_add_u64 v[66:67], v[36:37], 0, v[114:115]
	s_nop 0
	v_addc_co_u32_e32 v69, vcc, 0, v3, vcc
	ds_read_b128 v[4:7], v88
	ds_read_b128 v[8:11], v88 offset:6400
	global_load_dwordx4 v[12:15], v[2:3], off
	global_load_dwordx4 v[28:31], v[64:65], off
	global_load_dwordx4 v[40:43], v[62:63], off offset:2048
	global_load_dwordx4 v[48:51], v[66:67], off
	global_load_dwordx4 v[56:59], v[68:69], off offset:2048
	v_cmp_lt_i32_e32 vcc, v98, v96
	global_load_dwordx4 v[20:23], v[20:21], off offset:2048
	global_load_dwordx4 v[140:143], v[2:3], off offset:64
	global_load_dwordx4 v[144:147], v[38:39], off offset:64
	global_load_dwordx4 v[148:151], v[64:65], off offset:64
	global_load_dwordx4 v[152:155], v[62:63], off offset:2112
	global_load_dwordx4 v[156:159], v[66:67], off offset:64
	global_load_dwordx4 v[160:163], v[68:69], off offset:2112
	global_load_dwordx4 v[164:167], v[2:3], off offset:128
	global_load_dwordx4 v[168:171], v[38:39], off offset:128
	global_load_dwordx4 v[172:175], v[64:65], off offset:128
	global_load_dwordx4 v[176:179], v[62:63], off offset:2176
	global_load_dwordx4 v[180:183], v[66:67], off offset:128
	global_load_dwordx4 v[184:187], v[68:69], off offset:2176
	global_load_dwordx4 v[188:191], v[2:3], off offset:192
	global_load_dwordx4 v[192:195], v[38:39], off offset:192
	global_load_dwordx4 v[196:199], v[64:65], off offset:192
	global_load_dwordx4 v[200:203], v[62:63], off offset:2240
	global_load_dwordx4 v[204:207], v[66:67], off offset:192
	global_load_dwordx4 v[208:211], v[68:69], off offset:2240
	global_load_dwordx4 v[212:215], v[2:3], off offset:256
	global_load_dwordx4 v[216:219], v[38:39], off offset:256
	global_load_dwordx4 v[220:223], v[66:67], off offset:256
	global_load_dwordx4 v[234:237], v[64:65], off offset:256
	global_load_dwordx4 v[238:241], v[62:63], off offset:2304
	global_load_dwordx4 v[242:245], v[68:69], off offset:2304
	s_lshl_b32 s0, s2, 2
	s_add_i32 s0, s91, s0
	s_ashr_i32 s1, s0, 31
	s_ashr_i32 s2, s16, 31
	s_lshl_b64 s[0:1], s[0:1], 13
	s_waitcnt vmcnt(29) lgkmcnt(1)
	v_mfma_f32_16x16x32_bf16 v[16:19], v[12:15], v[4:7], 0
	s_waitcnt lgkmcnt(0)
	v_mfma_f32_16x16x32_bf16 v[12:15], v[12:15], v[8:11], 0
	s_waitcnt vmcnt(24)
	v_mfma_f32_16x16x32_bf16 v[24:27], v[20:23], v[4:7], 0
	v_mfma_f32_16x16x32_bf16 v[20:23], v[20:23], v[8:11], 0
	v_mfma_f32_16x16x32_bf16 v[32:35], v[28:31], v[4:7], 0
	v_mfma_f32_16x16x32_bf16 v[28:31], v[28:31], v[8:11], 0
	v_mfma_f32_16x16x32_bf16 v[44:47], v[40:43], v[4:7], 0
	v_mfma_f32_16x16x32_bf16 v[40:43], v[40:43], v[8:11], 0
	v_mfma_f32_16x16x32_bf16 v[52:55], v[48:51], v[4:7], 0
	v_mfma_f32_16x16x32_bf16 v[48:51], v[48:51], v[8:11], 0
	v_mfma_f32_16x16x32_bf16 v[4:7], v[56:59], v[4:7], 0
	v_mfma_f32_16x16x32_bf16 v[8:11], v[56:59], v[8:11], 0
	ds_read_b128 v[56:59], v88 offset:64
	ds_read_b128 v[70:73], v88 offset:6464
	s_waitcnt vmcnt(23) lgkmcnt(1)
	v_mfma_f32_16x16x32_bf16 v[16:19], v[140:143], v[56:59], v[16:19]
	s_waitcnt lgkmcnt(0)
	v_mfma_f32_16x16x32_bf16 v[12:15], v[140:143], v[70:73], v[12:15]
	s_waitcnt vmcnt(22)
	v_mfma_f32_16x16x32_bf16 v[24:27], v[144:147], v[56:59], v[24:27]
	v_mfma_f32_16x16x32_bf16 v[20:23], v[144:147], v[70:73], v[20:23]
	s_waitcnt vmcnt(21)
	v_mfma_f32_16x16x32_bf16 v[32:35], v[148:151], v[56:59], v[32:35]
	v_mfma_f32_16x16x32_bf16 v[28:31], v[148:151], v[70:73], v[28:31]
	s_waitcnt vmcnt(20)
	v_mfma_f32_16x16x32_bf16 v[44:47], v[152:155], v[56:59], v[44:47]
	v_mfma_f32_16x16x32_bf16 v[40:43], v[152:155], v[70:73], v[40:43]
	s_waitcnt vmcnt(19)
	v_mfma_f32_16x16x32_bf16 v[52:55], v[156:159], v[56:59], v[52:55]
	v_mfma_f32_16x16x32_bf16 v[48:51], v[156:159], v[70:73], v[48:51]
	s_waitcnt vmcnt(18)
	v_mfma_f32_16x16x32_bf16 v[4:7], v[160:163], v[56:59], v[4:7]
	v_mfma_f32_16x16x32_bf16 v[8:11], v[160:163], v[70:73], v[8:11]
	global_load_dwordx4 v[140:143], v[2:3], off offset:320
	global_load_dwordx4 v[144:147], v[38:39], off offset:320
	global_load_dwordx4 v[148:151], v[64:65], off offset:320
	global_load_dwordx4 v[152:155], v[62:63], off offset:2368
	global_load_dwordx4 v[156:159], v[66:67], off offset:320
	global_load_dwordx4 v[160:163], v[68:69], off offset:2368
	ds_read_b128 v[56:59], v88 offset:128
	ds_read_b128 v[70:73], v88 offset:6528
	s_waitcnt vmcnt(23) lgkmcnt(1)
	v_mfma_f32_16x16x32_bf16 v[16:19], v[164:167], v[56:59], v[16:19]
	s_waitcnt lgkmcnt(0)
	v_mfma_f32_16x16x32_bf16 v[12:15], v[164:167], v[70:73], v[12:15]
	s_waitcnt vmcnt(22)
	v_mfma_f32_16x16x32_bf16 v[24:27], v[168:171], v[56:59], v[24:27]
	v_mfma_f32_16x16x32_bf16 v[20:23], v[168:171], v[70:73], v[20:23]
	s_waitcnt vmcnt(21)
	v_mfma_f32_16x16x32_bf16 v[32:35], v[172:175], v[56:59], v[32:35]
	v_mfma_f32_16x16x32_bf16 v[28:31], v[172:175], v[70:73], v[28:31]
	s_waitcnt vmcnt(20)
	v_mfma_f32_16x16x32_bf16 v[44:47], v[176:179], v[56:59], v[44:47]
	v_mfma_f32_16x16x32_bf16 v[40:43], v[176:179], v[70:73], v[40:43]
	s_waitcnt vmcnt(19)
	v_mfma_f32_16x16x32_bf16 v[52:55], v[180:183], v[56:59], v[52:55]
	v_mfma_f32_16x16x32_bf16 v[48:51], v[180:183], v[70:73], v[48:51]
	s_waitcnt vmcnt(18)
	v_mfma_f32_16x16x32_bf16 v[4:7], v[184:187], v[56:59], v[4:7]
	v_mfma_f32_16x16x32_bf16 v[8:11], v[184:187], v[70:73], v[8:11]
	ds_read_b128 v[56:59], v88 offset:192
	ds_read_b128 v[70:73], v88 offset:6592
	s_waitcnt vmcnt(17) lgkmcnt(1)
	v_mfma_f32_16x16x32_bf16 v[16:19], v[188:191], v[56:59], v[16:19]
	s_waitcnt lgkmcnt(0)
	v_mfma_f32_16x16x32_bf16 v[12:15], v[188:191], v[70:73], v[12:15]
	s_waitcnt vmcnt(16)
	v_mfma_f32_16x16x32_bf16 v[24:27], v[192:195], v[56:59], v[24:27]
	v_mfma_f32_16x16x32_bf16 v[20:23], v[192:195], v[70:73], v[20:23]
	s_waitcnt vmcnt(15)
	v_mfma_f32_16x16x32_bf16 v[32:35], v[196:199], v[56:59], v[32:35]
	v_mfma_f32_16x16x32_bf16 v[28:31], v[196:199], v[70:73], v[28:31]
	s_waitcnt vmcnt(14)
	v_mfma_f32_16x16x32_bf16 v[44:47], v[200:203], v[56:59], v[44:47]
	v_mfma_f32_16x16x32_bf16 v[40:43], v[200:203], v[70:73], v[40:43]
	s_waitcnt vmcnt(13)
	v_mfma_f32_16x16x32_bf16 v[84:87], v[204:207], v[56:59], v[52:55]
	s_nop 2
	ds_read_b128 v[100:103], v88 offset:256
	ds_read_b128 v[104:107], v88 offset:6656
	v_mfma_f32_16x16x32_bf16 v[48:51], v[204:207], v[70:73], v[48:51]
	s_waitcnt vmcnt(12)
	v_mfma_f32_16x16x32_bf16 v[74:77], v[208:211], v[56:59], v[4:7]
	s_nop 2
	s_waitcnt vmcnt(11) lgkmcnt(1)
	v_mfma_f32_16x16x32_bf16 v[108:111], v[212:215], v[100:103], v[16:19]
	s_waitcnt lgkmcnt(0)
	v_mfma_f32_16x16x32_bf16 v[116:119], v[212:215], v[104:107], v[12:15]
	v_mfma_f32_16x16x32_bf16 v[70:73], v[208:211], v[70:73], v[8:11]
	s_nop 2
	s_waitcnt vmcnt(10)
	v_mfma_f32_16x16x32_bf16 v[14:17], v[216:219], v[100:103], v[24:27]
	v_mfma_f32_16x16x32_bf16 v[58:61], v[216:219], v[104:107], v[20:23]
	s_waitcnt vmcnt(8)
	v_mfma_f32_16x16x32_bf16 v[22:25], v[234:237], v[100:103], v[32:35]
	v_mfma_f32_16x16x32_bf16 v[54:57], v[234:237], v[104:107], v[28:31]
	s_nop 1
	s_waitcnt vmcnt(7)
	v_mfma_f32_16x16x32_bf16 v[18:21], v[238:241], v[100:103], v[44:47]
	v_mfma_f32_16x16x32_bf16 v[26:29], v[238:241], v[104:107], v[40:43]
	v_mfma_f32_16x16x32_bf16 v[50:53], v[220:223], v[104:107], v[48:51]
	ds_read_b128 v[34:37], v88 offset:320
	s_nop 1
	ds_read_b128 v[46:49], v88 offset:6720
	s_waitcnt vmcnt(6)
	v_mfma_f32_16x16x32_bf16 v[42:45], v[242:245], v[104:107], v[70:73]
	s_nop 2
	s_waitcnt vmcnt(4) lgkmcnt(1)
	v_mfma_f32_16x16x32_bf16 v[38:41], v[144:147], v[34:37], v[14:17]
	s_waitcnt lgkmcnt(0)
	v_mfma_f32_16x16x32_bf16 v[14:17], v[144:147], v[46:49], v[58:61]
	s_nop 0
	s_waitcnt vmcnt(3)
	v_mfma_f32_16x16x32_bf16 v[58:61], v[148:151], v[34:37], v[22:25]
	v_mfma_f32_16x16x32_bf16 v[22:25], v[148:151], v[46:49], v[54:57]
	s_waitcnt vmcnt(2)
	v_mfma_f32_16x16x32_bf16 v[54:57], v[152:155], v[34:37], v[18:21]
	v_mfma_f32_16x16x32_bf16 v[18:21], v[152:155], v[46:49], v[26:29]
	v_mfma_f32_16x16x32_bf16 v[6:9], v[220:223], v[100:103], v[84:87]
	s_waitcnt vmcnt(1)
	v_mfma_f32_16x16x32_bf16 v[26:29], v[156:159], v[34:37], v[6:9]
	v_mfma_f32_16x16x32_bf16 v[6:9], v[156:159], v[46:49], v[50:53]
	s_nop 2
	v_mfma_f32_16x16x32_bf16 v[10:13], v[242:245], v[100:103], v[74:77]
	v_mfma_f32_16x16x32_bf16 v[30:33], v[140:143], v[34:37], v[108:111]
	v_mfma_f32_16x16x32_bf16 v[2:5], v[140:143], v[46:49], v[116:119]
	s_waitcnt vmcnt(0)
	v_mfma_f32_16x16x32_bf16 v[34:37], v[160:163], v[34:37], v[10:13]
	v_mfma_f32_16x16x32_bf16 v[10:13], v[160:163], v[46:49], v[42:45]
	s_nop 3
	v_mul_f32_e32 v46, v31, v31
	v_fmac_f32_e32 v46, v30, v30
	v_fmac_f32_e32 v46, v32, v32
	v_fmac_f32_e32 v46, v33, v33
	v_fmac_f32_e32 v46, v38, v38
	v_fmac_f32_e32 v46, v39, v39
	v_fmac_f32_e32 v46, v40, v40
	v_fmac_f32_e32 v46, v41, v41
	v_fmac_f32_e32 v46, v58, v58
	v_fmac_f32_e32 v46, v59, v59
	v_fmac_f32_e32 v46, v60, v60
	v_fmac_f32_e32 v46, v61, v61
	v_fmac_f32_e32 v46, v54, v54
	v_fmac_f32_e32 v46, v55, v55
	v_fmac_f32_e32 v46, v56, v56
	v_fmac_f32_e32 v46, v57, v57
	v_fmac_f32_e32 v46, v26, v26
	v_fmac_f32_e32 v46, v27, v27
	v_pk_mul_f32 v[44:45], v[28:29], v[28:29]
	v_cndmask_b32_e32 v42, v228, v98, vcc
	v_add_f32_e32 v44, v44, v46
	v_add_f32_e32 v48, v45, v44
	v_pk_mul_f32 v[46:47], v[34:35], v[34:35]
	v_pk_mul_f32 v[44:45], v[36:37], v[36:37]
	v_add_f32_e32 v46, v46, v48
	v_add_f32_e32 v46, v47, v46
	v_add_f32_e32 v44, v44, v46
	v_lshlrev_b32_e32 v69, 2, v42
	v_add_f32_e32 v44, v45, v44
	ds_bpermute_b32 v45, v69, v44
	v_cmp_lt_i32_e32 vcc, v97, v96
	v_mov_b32_e32 v43, s2
	s_waitcnt lgkmcnt(0)
	v_add_f32_e32 v44, v44, v45
	v_cndmask_b32_e32 v42, v228, v97, vcc
	v_lshlrev_b32_e32 v86, 2, v42
	ds_bpermute_b32 v45, v86, v44
	v_or_b32_e32 v42, s16, v91
	v_lshl_add_u64 v[64:65], v[42:43], 0, s[0:1]
	v_readlane_b32 s0, v253, 11
	v_lshlrev_b64 v[42:43], 2, v[78:79]
	s_waitcnt lgkmcnt(0)
	v_add_f32_e32 v44, v44, v45
	v_fmamk_f32 v44, v44, 0x3c2aaaab, v225
	v_rsq_f32_e32 v44, v44
	v_readlane_b32 s1, v253, 12
	v_lshl_add_u64 v[62:63], s[34:35], 0, v[42:43]
	global_load_dwordx4 v[46:49], v[62:63], off offset:320
	v_lshl_add_u64 v[52:53], s[0:1], 0, v[42:43]
	v_readlane_b32 s0, v253, 13
	v_readlane_b32 s1, v253, 14
	v_mul_f32_e32 v68, 0x3e16c740, v44
	v_pk_mul_f32 v[30:31], v[30:31], v[68:69] op_sel_hi:[1,0]
	v_lshl_add_u64 v[50:51], s[0:1], 0, v[42:43]
	global_load_dwordx4 v[42:45], v[62:63], off
	v_pk_mul_f32 v[38:39], v[38:39], v[68:69] op_sel_hi:[1,0]
	v_pk_mul_f32 v[34:35], v[34:35], v[68:69] op_sel_hi:[1,0]
	v_pk_mul_f32 v[26:27], v[26:27], v[68:69] op_sel_hi:[1,0]
	v_readlane_b32 s0, v253, 19
	v_readlane_b32 s1, v253, 20
	s_waitcnt vmcnt(1)
	v_pk_mul_f32 v[34:35], v[34:35], v[46:47]
	v_lshl_add_u64 v[66:67], v[78:79], 1, s[0:1]
	s_waitcnt vmcnt(0)
	v_pk_mul_f32 v[72:73], v[42:43], v[30:31]
	v_pk_mul_f32 v[30:31], v[32:33], v[68:69] op_sel_hi:[1,0]
	s_nop 0
	v_pk_mul_f32 v[70:71], v[44:45], v[30:31]
	global_load_dwordx4 v[30:33], v[62:63], off offset:64
	global_load_dwordx4 v[42:45], v[62:63], off offset:256
	s_waitcnt vmcnt(1)
	v_pk_mul_f32 v[76:77], v[30:31], v[38:39]
	v_pk_mul_f32 v[30:31], v[40:41], v[68:69] op_sel_hi:[1,0]
	v_pk_mul_f32 v[38:39], v[58:59], v[68:69] op_sel_hi:[1,0]
	v_pk_mul_f32 v[74:75], v[32:33], v[30:31]
	global_load_dwordx4 v[30:33], v[62:63], off offset:128
	s_waitcnt vmcnt(1)
	v_pk_mul_f32 v[26:27], v[26:27], v[42:43]
	s_waitcnt vmcnt(0)
	v_pk_mul_f32 v[84:85], v[30:31], v[38:39]
	v_pk_mul_f32 v[30:31], v[60:61], v[68:69] op_sel_hi:[1,0]
	v_pk_mul_f32 v[38:39], v[54:55], v[68:69] op_sel_hi:[1,0]
	v_pk_mul_f32 v[58:59], v[32:33], v[30:31]
	global_load_dwordx4 v[30:33], v[62:63], off offset:192
	s_waitcnt vmcnt(0)
	v_pk_mul_f32 v[60:61], v[30:31], v[38:39]
	v_pk_mul_f32 v[30:31], v[56:57], v[68:69] op_sel_hi:[1,0]
	v_lshlrev_b64 v[38:39], 6, v[80:81]
	v_pk_mul_f32 v[54:55], v[32:33], v[30:31]
	v_lshl_add_u64 v[30:31], v[52:53], 0, v[38:39]
	v_lshl_add_u64 v[38:39], v[50:51], 0, v[38:39]
	global_load_dwordx4 v[30:33], v[30:31], off
	s_nop 0
	global_load_dwordx4 v[38:41], v[38:39], off
	s_waitcnt vmcnt(0)
	v_pk_mul_f32 v[42:43], v[34:35], v[38:39]
	s_nop 0
	v_pk_fma_f32 v[42:43], v[26:27], v[30:31], v[42:43] neg_lo:[0,0,1] neg_hi:[0,0,1]
	v_pk_mul_f32 v[26:27], v[26:27], v[38:39]
	s_nop 0
	v_pk_fma_f32 v[30:31], v[34:35], v[30:31], v[26:27]
	v_pk_mul_f32 v[26:27], v[28:29], v[68:69] op_sel_hi:[1,0]
	v_pk_mul_f32 v[28:29], v[36:37], v[68:69] op_sel_hi:[1,0]
	v_pk_mul_f32 v[26:27], v[26:27], v[44:45]
	v_pk_mul_f32 v[28:29], v[28:29], v[48:49]
	v_cvt_pk_bf16_f32 v30, v30, v31
	v_pk_mul_f32 v[34:35], v[28:29], v[40:41]
	s_nop 0
	v_pk_fma_f32 v[34:35], v[26:27], v[32:33], v[34:35] neg_lo:[0,0,1] neg_hi:[0,0,1]
	v_pk_mul_f32 v[26:27], v[26:27], v[40:41]
	s_nop 0
	v_pk_fma_f32 v[28:29], v[28:29], v[32:33], v[26:27]
	v_mad_u64_u32 v[26:27], s[0:1], v64, s8, v[66:67]
	v_mad_i32_i24 v27, v65, s8, v27
	v_cvt_pk_bf16_f32 v31, v28, v29
	global_store_dwordx2 v[26:27], v[30:31], off offset:160
	v_mul_f32_e32 v30, v3, v3
	v_fmac_f32_e32 v30, v2, v2
	v_fmac_f32_e32 v30, v4, v4
	v_fmac_f32_e32 v30, v5, v5
	v_fmac_f32_e32 v30, v14, v14
	v_fmac_f32_e32 v30, v15, v15
	v_fmac_f32_e32 v30, v16, v16
	v_fmac_f32_e32 v30, v17, v17
	v_fmac_f32_e32 v30, v22, v22
	v_fmac_f32_e32 v30, v23, v23
	v_fmac_f32_e32 v30, v24, v24
	v_fmac_f32_e32 v30, v25, v25
	v_fmac_f32_e32 v30, v18, v18
	v_fmac_f32_e32 v30, v19, v19
	v_cvt_pk_bf16_f32 v32, v72, v73
	v_cvt_pk_bf16_f32 v33, v70, v71
	v_fmac_f32_e32 v30, v20, v20
	global_store_dwordx2 v[26:27], v[32:33], off
	v_cvt_pk_bf16_f32 v32, v76, v77
	v_cvt_pk_bf16_f32 v33, v74, v75
	v_fmac_f32_e32 v30, v21, v21
	global_store_dwordx2 v[26:27], v[32:33], off offset:32
	v_cvt_pk_bf16_f32 v32, v84, v85
	v_cvt_pk_bf16_f32 v33, v58, v59
	v_fmac_f32_e32 v30, v6, v6
	global_store_dwordx2 v[26:27], v[32:33], off offset:64
	v_cvt_pk_bf16_f32 v32, v60, v61
	v_cvt_pk_bf16_f32 v33, v54, v55
	v_fmac_f32_e32 v30, v7, v7
	v_pk_mul_f32 v[28:29], v[8:9], v[8:9]
	global_store_dwordx2 v[26:27], v[32:33], off offset:96
	v_cvt_pk_bf16_f32 v32, v42, v43
	v_cvt_pk_bf16_f32 v33, v34, v35
	v_add_f32_e32 v28, v28, v30
	global_store_dwordx2 v[26:27], v[32:33], off offset:128
	v_add_f32_e32 v32, v29, v28
	v_pk_mul_f32 v[30:31], v[10:11], v[10:11]
	v_pk_mul_f32 v[28:29], v[12:13], v[12:13]
	v_add_f32_e32 v30, v30, v32
	v_add_f32_e32 v30, v31, v30
	v_add_f32_e32 v28, v28, v30
	global_load_dwordx4 v[30:33], v[62:63], off
	global_load_dwordx4 v[42:45], v[62:63], off offset:320
	v_add_f32_e32 v28, v29, v28
	ds_bpermute_b32 v29, v69, v28
	s_waitcnt lgkmcnt(0)
	v_add_f32_e32 v28, v28, v29
	ds_bpermute_b32 v29, v86, v28
	s_waitcnt lgkmcnt(0)
	v_add_f32_e32 v28, v28, v29
	v_fmamk_f32 v28, v28, 0x3c2aaaab, v225
	v_rsq_f32_e32 v28, v28
	s_nop 0
	v_mul_f32_e32 v28, 0x3e16c740, v28
	v_pk_mul_f32 v[2:3], v[2:3], v[28:29] op_sel_hi:[1,0]
	v_pk_mul_f32 v[14:15], v[14:15], v[28:29] op_sel_hi:[1,0]
	v_pk_mul_f32 v[10:11], v[10:11], v[28:29] op_sel_hi:[1,0]
	v_pk_mul_f32 v[6:7], v[6:7], v[28:29] op_sel_hi:[1,0]
	s_waitcnt vmcnt(1)
	v_pk_mul_f32 v[30:31], v[30:31], v[2:3]
	v_pk_mul_f32 v[2:3], v[4:5], v[28:29] op_sel_hi:[1,0]
	s_waitcnt vmcnt(0)
	v_pk_mul_f32 v[10:11], v[10:11], v[42:43]
	v_pk_mul_f32 v[32:33], v[32:33], v[2:3]
	global_load_dwordx4 v[2:5], v[62:63], off offset:64
	s_waitcnt vmcnt(0)
	v_pk_mul_f32 v[34:35], v[2:3], v[14:15]
	v_pk_mul_f32 v[2:3], v[16:17], v[28:29] op_sel_hi:[1,0]
	v_pk_mul_f32 v[14:15], v[22:23], v[28:29] op_sel_hi:[1,0]
	v_pk_mul_f32 v[36:37], v[4:5], v[2:3]
	global_load_dwordx4 v[2:5], v[62:63], off offset:128
	s_waitcnt vmcnt(0)
	v_pk_mul_f32 v[22:23], v[14:15], v[2:3]
	v_pk_mul_f32 v[2:3], v[24:25], v[28:29] op_sel_hi:[1,0]
	v_pk_mul_f32 v[14:15], v[18:19], v[28:29] op_sel_hi:[1,0]
	v_pk_mul_f32 v[24:25], v[2:3], v[4:5]
	global_load_dwordx4 v[2:5], v[62:63], off offset:192
	s_waitcnt vmcnt(0)
	v_pk_mul_f32 v[38:39], v[14:15], v[2:3]
	v_pk_mul_f32 v[2:3], v[20:21], v[28:29] op_sel_hi:[1,0]
	global_load_dwordx4 v[18:21], v[62:63], off offset:256
	v_pk_mul_f32 v[40:41], v[2:3], v[4:5]
	v_or_b32_e32 v2, 16, v80
	v_ashrrev_i32_e32 v3, 31, v2
	v_lshlrev_b64 v[14:15], 6, v[2:3]
	v_lshl_add_u64 v[2:3], v[52:53], 0, v[14:15]
	v_lshl_add_u64 v[14:15], v[50:51], 0, v[14:15]
	global_load_dwordx4 v[2:5], v[2:3], off
	s_waitcnt vmcnt(1)
	v_pk_mul_f32 v[6:7], v[6:7], v[18:19]
	global_load_dwordx4 v[14:17], v[14:15], off
	s_waitcnt vmcnt(0)
	v_pk_mul_f32 v[18:19], v[10:11], v[14:15]
	s_nop 0
	v_pk_fma_f32 v[18:19], v[6:7], v[2:3], v[18:19] neg_lo:[0,0,1] neg_hi:[0,0,1]
	v_pk_mul_f32 v[6:7], v[6:7], v[14:15]
	s_nop 0
	v_pk_fma_f32 v[2:3], v[10:11], v[2:3], v[6:7]
	v_pk_mul_f32 v[6:7], v[8:9], v[28:29] op_sel_hi:[1,0]
	v_pk_mul_f32 v[8:9], v[12:13], v[28:29] op_sel_hi:[1,0]
	v_pk_mul_f32 v[6:7], v[6:7], v[20:21]
	v_pk_mul_f32 v[8:9], v[8:9], v[44:45]
	v_cvt_pk_bf16_f32 v2, v2, v3
	v_pk_mul_f32 v[10:11], v[8:9], v[16:17]
	s_nop 0
	v_pk_fma_f32 v[10:11], v[6:7], v[4:5], v[10:11] neg_lo:[0,0,1] neg_hi:[0,0,1]
	v_pk_mul_f32 v[6:7], v[6:7], v[16:17]
	s_nop 0
	v_pk_fma_f32 v[4:5], v[8:9], v[4:5], v[6:7]
	v_cvt_pk_bf16_f32 v6, v30, v31
	v_cvt_pk_bf16_f32 v7, v32, v33
	global_store_dwordx2 v[26:27], v[6:7], off offset:3072
	v_cvt_pk_bf16_f32 v6, v34, v35
	v_cvt_pk_bf16_f32 v7, v36, v37
	global_store_dwordx2 v[26:27], v[6:7], off offset:3104
	v_cvt_pk_bf16_f32 v6, v22, v23
	v_cvt_pk_bf16_f32 v7, v24, v25
	global_store_dwordx2 v[26:27], v[6:7], off offset:3136
	v_cvt_pk_bf16_f32 v6, v38, v39
	v_cvt_pk_bf16_f32 v7, v40, v41
	global_store_dwordx2 v[26:27], v[6:7], off offset:3168
	v_cvt_pk_bf16_f32 v6, v18, v19
	v_cvt_pk_bf16_f32 v7, v10, v11
	v_cvt_pk_bf16_f32 v3, v4, v5
	global_store_dwordx2 v[26:27], v[6:7], off offset:3200
	global_store_dwordx2 v[26:27], v[2:3], off offset:3232

.LBB0_1001:
	v_add_u32_e32 v229, s22, v181
	v_add_u32_e32 v231, s22, v198
	ds_read_b128 v[66:69], v229 offset:17408
	ds_read_b128 v[70:73], v229
	ds_read_b128 v[82:85], v231 offset:8704
	ds_read_b128 v[86:89], v231 offset:8976
	ds_read_b128 v[90:93], v231
	ds_read_b128 v[94:97], v231 offset:272
	ds_read_b128 v[234:237], v231 offset:9248
	ds_read_b128 v[238:241], v231 offset:9520
	ds_read_b128 v[242:245], v231 offset:544
	ds_read_b128 v[246:249], v231 offset:816
	s_waitcnt lgkmcnt(4)
	v_sub_f32_e32 v220, v70, v94
	v_sub_f32_e32 v221, v70, v90
	v_exp_f32_e32 v164, v220
	v_exp_f32_e32 v165, v221
	v_sub_f32_e32 v222, v71, v95
	v_sub_f32_e32 v223, v71, v91
	v_exp_f32_e32 v166, v222
	v_exp_f32_e32 v167, v223
	v_sub_f32_e32 v220, v72, v96
	v_sub_f32_e32 v221, v72, v92
	v_exp_f32_e32 v216, v220
	v_exp_f32_e32 v217, v221
	v_sub_f32_e32 v222, v73, v97
	v_sub_f32_e32 v223, v73, v93
	v_exp_f32_e32 v218, v222
	v_exp_f32_e32 v219, v223
	v_mov_b32_e32 v90, v86
	v_mov_b32_e32 v91, v82
	v_mov_b32_e32 v92, v87
	v_mov_b32_e32 v93, v83
	v_mov_b32_e32 v94, v88
	v_mov_b32_e32 v95, v84
	v_mov_b32_e32 v96, v89
	v_mov_b32_e32 v97, v85
	v_pk_mul_f32 v[90:91], v[66:67], v[90:91] op_sel_hi:[0,1]
	v_pk_mul_f32 v[92:93], v[66:67], v[92:93] op_sel:[1,0]
	v_pk_fma_f32 v[80:81], v[90:91], v[164:165], v[80:81]
	v_pk_mul_f32 v[94:95], v[68:69], v[94:95] op_sel_hi:[0,1]
	v_pk_fma_f32 v[80:81], v[92:93], v[166:167], v[80:81]
	v_pk_mul_f32 v[96:97], v[68:69], v[96:97] op_sel:[1,0]
	v_pk_fma_f32 v[80:81], v[94:95], v[216:217], v[80:81]
	s_nop 0
	v_pk_fma_f32 v[80:81], v[96:97], v[218:219], v[80:81]
	ds_read_b128 v[82:85], v231 offset:9792
	ds_read_b128 v[86:89], v231 offset:10064
	ds_read_b128 v[90:93], v231 offset:1088
	ds_read_b128 v[94:97], v231 offset:1360
	s_waitcnt lgkmcnt(4)
	v_sub_f32_e32 v220, v70, v246
	v_sub_f32_e32 v221, v70, v242
	v_exp_f32_e32 v164, v220
	v_exp_f32_e32 v165, v221
	v_sub_f32_e32 v222, v71, v247
	v_sub_f32_e32 v223, v71, v243
	v_exp_f32_e32 v166, v222
	v_exp_f32_e32 v167, v223
	v_sub_f32_e32 v220, v72, v248
	v_sub_f32_e32 v221, v72, v244
	v_exp_f32_e32 v216, v220
	v_exp_f32_e32 v217, v221
	v_sub_f32_e32 v222, v73, v249
	v_sub_f32_e32 v223, v73, v245
	v_exp_f32_e32 v218, v222
	v_exp_f32_e32 v219, v223
	v_mov_b32_e32 v242, v238
	v_mov_b32_e32 v243, v234
	v_mov_b32_e32 v244, v239
	v_mov_b32_e32 v245, v235
	v_mov_b32_e32 v246, v240
	v_mov_b32_e32 v247, v236
	v_mov_b32_e32 v248, v241
	v_mov_b32_e32 v249, v237
	v_pk_mul_f32 v[242:243], v[66:67], v[242:243] op_sel_hi:[0,1]
	v_pk_mul_f32 v[244:245], v[66:67], v[244:245] op_sel:[1,0]
	v_pk_fma_f32 v[78:79], v[242:243], v[164:165], v[78:79]
	v_pk_mul_f32 v[246:247], v[68:69], v[246:247] op_sel_hi:[0,1]
	v_pk_fma_f32 v[78:79], v[244:245], v[166:167], v[78:79]
	v_pk_mul_f32 v[248:249], v[68:69], v[248:249] op_sel:[1,0]
	v_pk_fma_f32 v[78:79], v[246:247], v[216:217], v[78:79]
	s_nop 0
	v_pk_fma_f32 v[78:79], v[248:249], v[218:219], v[78:79]
	ds_read_b128 v[234:237], v231 offset:10336
	ds_read_b128 v[238:241], v231 offset:10608
	ds_read_b128 v[242:245], v231 offset:1632
	ds_read_b128 v[246:249], v231 offset:1904
	s_waitcnt lgkmcnt(4)
	v_sub_f32_e32 v220, v70, v94
	v_sub_f32_e32 v221, v70, v90
	v_exp_f32_e32 v164, v220
	v_exp_f32_e32 v165, v221
	v_sub_f32_e32 v222, v71, v95
	v_sub_f32_e32 v223, v71, v91
	v_exp_f32_e32 v166, v222
	v_exp_f32_e32 v167, v223
	v_sub_f32_e32 v220, v72, v96
	v_sub_f32_e32 v221, v72, v92
	v_exp_f32_e32 v216, v220
	v_exp_f32_e32 v217, v221
	v_sub_f32_e32 v222, v73, v97
	v_sub_f32_e32 v223, v73, v93
	v_exp_f32_e32 v218, v222
	v_exp_f32_e32 v219, v223
	v_mov_b32_e32 v90, v86
	v_mov_b32_e32 v91, v82
	v_mov_b32_e32 v92, v87
	v_mov_b32_e32 v93, v83
	v_mov_b32_e32 v94, v88
	v_mov_b32_e32 v95, v84
	v_mov_b32_e32 v96, v89
	v_mov_b32_e32 v97, v85
	v_pk_mul_f32 v[90:91], v[66:67], v[90:91] op_sel_hi:[0,1]
	v_pk_mul_f32 v[92:93], v[66:67], v[92:93] op_sel:[1,0]
	v_pk_fma_f32 v[76:77], v[90:91], v[164:165], v[76:77]
	v_pk_mul_f32 v[94:95], v[68:69], v[94:95] op_sel_hi:[0,1]
	v_pk_fma_f32 v[76:77], v[92:93], v[166:167], v[76:77]
	v_pk_mul_f32 v[96:97], v[68:69], v[96:97] op_sel:[1,0]
	v_pk_fma_f32 v[76:77], v[94:95], v[216:217], v[76:77]
	s_nop 0
	v_pk_fma_f32 v[76:77], v[96:97], v[218:219], v[76:77]
	s_waitcnt lgkmcnt(0)
	v_sub_f32_e32 v220, v70, v246
	v_sub_f32_e32 v221, v70, v242
	v_exp_f32_e32 v164, v220
	v_exp_f32_e32 v165, v221
	v_sub_f32_e32 v222, v71, v247
	v_sub_f32_e32 v223, v71, v243
	v_exp_f32_e32 v166, v222
	v_exp_f32_e32 v167, v223
	v_sub_f32_e32 v220, v72, v248
	v_sub_f32_e32 v221, v72, v244
	v_exp_f32_e32 v216, v220
	v_exp_f32_e32 v217, v221
	v_sub_f32_e32 v222, v73, v249
	v_sub_f32_e32 v223, v73, v245
	v_exp_f32_e32 v218, v222
	v_exp_f32_e32 v219, v223
	v_mov_b32_e32 v242, v238
	v_mov_b32_e32 v243, v234
	v_mov_b32_e32 v244, v239
	v_mov_b32_e32 v245, v235
	v_mov_b32_e32 v246, v240
	v_mov_b32_e32 v247, v236
	v_mov_b32_e32 v248, v241
	v_mov_b32_e32 v249, v237
	v_pk_mul_f32 v[242:243], v[66:67], v[242:243] op_sel_hi:[0,1]
	v_pk_mul_f32 v[244:245], v[66:67], v[244:245] op_sel:[1,0]
	v_pk_fma_f32 v[74:75], v[242:243], v[164:165], v[74:75]
	v_pk_mul_f32 v[246:247], v[68:69], v[246:247] op_sel_hi:[0,1]
	v_pk_fma_f32 v[74:75], v[244:245], v[166:167], v[74:75]
	v_pk_mul_f32 v[248:249], v[68:69], v[248:249] op_sel:[1,0]
	v_pk_fma_f32 v[74:75], v[246:247], v[216:217], v[74:75]
	s_nop 0
	v_pk_fma_f32 v[74:75], v[248:249], v[218:219], v[74:75]
	s_add_i32 s22, s22, 16
	s_cmpk_eq_i32 s22, 0x100
	s_cbranch_scc0 .LBB0_1001
	v_cndmask_b32_e64 v66, v81, 0, s[42:43]
	v_cndmask_b32_e64 v67, 0, v80, s[44:45]
	v_cndmask_b32_e64 v68, v79, 0, s[46:47]
	v_cndmask_b32_e64 v69, v78, 0, s[48:49]
	v_cndmask_b32_e64 v70, v77, 0, s[50:51]
	v_cndmask_b32_e64 v71, v76, 0, s[52:53]
	v_cndmask_b32_e64 v72, v75, 0, s[54:55]
	v_cndmask_b32_e64 v73, v74, 0, s[56:57]
	v_cvt_pk_bf16_f32 v216, v66, v67
	s_nop 1
	v_cvt_pk_bf16_f32 v217, v68, v69
	s_nop 1
	v_cvt_pk_bf16_f32 v218, v70, v71
	s_nop 1
	v_cvt_pk_bf16_f32 v219, v72, v73
	s_nop 1
	ds_read_b128 v[66:69], v185
	ds_read_b128 v[70:73], v185 offset:16
	ds_read_b128 v[74:77], v186
	ds_read_b128 v[78:81], v186 offset:16
	ds_read_b128 v[82:85], v187 offset:4080
	ds_read_b128 v[86:89], v187 offset:4096
	s_add_i32 s0, s0, 1
	s_cmp_eq_u32 s0, 4
	s_waitcnt lgkmcnt(1)
	v_sub_f32_e32 v74, v74, v82
	v_cndmask_b32_e64 v74, v74, -v74, s[38:39]
	v_exp_f32_e32 v74, v74
	s_waitcnt lgkmcnt(0)
	v_sub_f32_e32 v78, v78, v86
	v_mul_f32_e32 v66, v66, v74
	v_cndmask_b32_e64 v74, v78, -v78, s[38:39]
	v_exp_f32_e32 v74, v74
	s_nop 0
	v_mul_f32_e32 v70, v70, v74
	v_sub_f32_e32 v74, v75, v83
	v_cndmask_b32_e64 v74, v74, -v74, s[38:39]
	v_exp_f32_e32 v74, v74
	v_sub_f32_e32 v75, v79, v87
	v_mul_f32_e32 v67, v67, v74
	v_cndmask_b32_e64 v74, v75, -v75, s[38:39]
	v_exp_f32_e32 v74, v74
	v_sub_f32_e32 v75, v80, v88
	v_mul_f32_e32 v71, v71, v74
	v_sub_f32_e32 v74, v76, v84
	v_cndmask_b32_e64 v74, v74, -v74, s[38:39]
	v_exp_f32_e32 v74, v74
	s_nop 0
	v_mul_f32_e32 v68, v68, v74
	v_cndmask_b32_e64 v74, v75, -v75, s[38:39]
	v_exp_f32_e32 v74, v74
	v_sub_f32_e32 v75, v81, v89
	v_mul_f32_e32 v72, v72, v74
	v_sub_f32_e32 v74, v77, v85
	v_cndmask_b32_e64 v74, v74, -v74, s[38:39]
	v_exp_f32_e32 v74, v74
	s_nop 0
	v_mul_f32_e32 v69, v69, v74
	v_cndmask_b32_e64 v74, v75, -v75, s[38:39]
	v_exp_f32_e32 v74, v74
	s_nop 0
	v_mul_f32_e32 v73, v73, v74
	v_cvt_pk_bf16_f32 v74, v66, v67
	s_nop 1
	v_cvt_pk_bf16_f32 v75, v68, v69
	s_nop 1
	v_cvt_pk_bf16_f32 v76, v70, v71
	s_nop 1
	v_cvt_pk_bf16_f32 v73, v72, v73
	s_nop 1
	ds_read_b128 v[82:85], v185 offset:64
	ds_read_b128 v[86:89], v185 offset:80
	ds_read_b128 v[90:93], v186 offset:64
	ds_read_b128 v[94:97], v186 offset:80
	ds_read_b128 v[164:167], v187 offset:4144
	ds_read_b128 v[220:223], v187 offset:4160
	v_cndmask_b32_e64 v66, 0, v74, s[38:39]
	v_cndmask_b32_e64 v67, 0, v75, s[38:39]
	v_cndmask_b32_e64 v68, 0, v76, s[38:39]
	s_waitcnt lgkmcnt(1)
	v_sub_f32_e32 v90, v90, v164
	v_cndmask_b32_e64 v90, v90, -v90, s[38:39]
	v_exp_f32_e32 v90, v90
	s_waitcnt lgkmcnt(0)
	v_sub_f32_e32 v94, v94, v220
	v_cndmask_b32_e64 v69, 0, v73, s[38:39]
	v_cndmask_b32_e64 v70, v74, 0, s[38:39]
	v_mul_f32_e32 v82, v82, v90
	v_cndmask_b32_e64 v90, v94, -v94, s[38:39]
	v_exp_f32_e32 v90, v90
	v_cndmask_b32_e64 v71, v75, 0, s[38:39]
	v_cndmask_b32_e64 v72, v76, 0, s[38:39]
	v_cndmask_b32_e64 v73, v73, 0, s[38:39]
	v_mul_f32_e32 v86, v86, v90
	v_sub_f32_e32 v90, v91, v165
	v_cndmask_b32_e64 v90, v90, -v90, s[38:39]
	v_exp_f32_e32 v90, v90
	v_sub_f32_e32 v91, v95, v221
	v_mfma_f32_32x32x16_bf16 v[66:81], v[66:69], v[70:73], 0
	v_mul_f32_e32 v83, v83, v90
	v_cndmask_b32_e64 v90, v91, -v91, s[38:39]
	v_exp_f32_e32 v90, v90
	v_sub_f32_e32 v91, v96, v222
	v_mul_f32_e32 v87, v87, v90
	v_sub_f32_e32 v90, v92, v166
	v_cndmask_b32_e64 v90, v90, -v90, s[38:39]
	v_exp_f32_e32 v90, v90
	s_nop 0
	v_mul_f32_e32 v84, v84, v90
	v_cndmask_b32_e64 v90, v91, -v91, s[38:39]
	v_exp_f32_e32 v90, v90
	v_sub_f32_e32 v91, v97, v223
	v_mul_f32_e32 v88, v88, v90
	v_sub_f32_e32 v90, v93, v167
	v_cndmask_b32_e64 v90, v90, -v90, s[38:39]
	v_exp_f32_e32 v90, v90
	s_nop 0
	v_mul_f32_e32 v85, v85, v90
	v_cndmask_b32_e64 v90, v91, -v91, s[38:39]
	v_exp_f32_e32 v90, v90
	s_nop 0
	v_mul_f32_e32 v89, v89, v90
	v_cvt_pk_bf16_f32 v90, v82, v83
	s_nop 1
	v_cvt_pk_bf16_f32 v91, v84, v85
	s_nop 1
	v_cvt_pk_bf16_f32 v92, v86, v87
	s_nop 1
	v_cvt_pk_bf16_f32 v89, v88, v89
	s_nop 1
	s_nop 0
	v_cndmask_b32_e64 v82, 0, v90, s[38:39]
	v_cndmask_b32_e64 v83, 0, v91, s[38:39]
	v_cndmask_b32_e64 v84, 0, v92, s[38:39]
	v_cndmask_b32_e64 v85, 0, v89, s[38:39]
	v_cndmask_b32_e64 v86, v90, 0, s[38:39]
	v_cndmask_b32_e64 v87, v91, 0, s[38:39]
	v_cndmask_b32_e64 v88, v92, 0, s[38:39]
	v_cndmask_b32_e64 v89, v89, 0, s[38:39]
	s_nop 1
	v_mfma_f32_32x32x16_bf16 v[66:81], v[82:85], v[86:89], v[66:81]
	ds_read_b128 v[82:85], v185 offset:128
	ds_read_b128 v[86:89], v185 offset:144
	ds_read_b128 v[90:93], v186 offset:128
	ds_read_b128 v[94:97], v186 offset:144
	ds_read_b128 v[164:167], v187 offset:4208
	ds_read_b128 v[220:223], v187 offset:4224
	s_waitcnt lgkmcnt(1)
	v_sub_f32_e32 v90, v90, v164
	v_cndmask_b32_e64 v90, v90, -v90, s[38:39]
	v_exp_f32_e32 v90, v90
	s_waitcnt lgkmcnt(0)
	v_sub_f32_e32 v94, v94, v220
	v_mul_f32_e32 v82, v82, v90
	v_cndmask_b32_e64 v90, v94, -v94, s[38:39]
	v_exp_f32_e32 v90, v90
	s_nop 0
	v_mul_f32_e32 v86, v86, v90
	v_sub_f32_e32 v90, v91, v165
	v_cndmask_b32_e64 v90, v90, -v90, s[38:39]
	v_exp_f32_e32 v90, v90
	v_sub_f32_e32 v91, v95, v221
	v_mul_f32_e32 v83, v83, v90
	v_cndmask_b32_e64 v90, v91, -v91, s[38:39]
	v_exp_f32_e32 v90, v90
	v_sub_f32_e32 v91, v96, v222
	v_mul_f32_e32 v87, v87, v90
	v_sub_f32_e32 v90, v92, v166
	v_cndmask_b32_e64 v90, v90, -v90, s[38:39]
	v_exp_f32_e32 v90, v90
	s_nop 0
	v_mul_f32_e32 v84, v84, v90
	v_cndmask_b32_e64 v90, v91, -v91, s[38:39]
	v_exp_f32_e32 v90, v90
	v_sub_f32_e32 v91, v97, v223
	v_mul_f32_e32 v88, v88, v90
	v_sub_f32_e32 v90, v93, v167
	v_cndmask_b32_e64 v90, v90, -v90, s[38:39]
	v_exp_f32_e32 v90, v90
	s_nop 0
	v_mul_f32_e32 v85, v85, v90
	v_cndmask_b32_e64 v90, v91, -v91, s[38:39]
	v_exp_f32_e32 v90, v90
	s_nop 0
	v_mul_f32_e32 v89, v89, v90
	v_cvt_pk_bf16_f32 v90, v82, v83
	s_nop 1
	v_cvt_pk_bf16_f32 v91, v84, v85
	s_nop 1
	v_cvt_pk_bf16_f32 v92, v86, v87
	s_nop 1
	v_cvt_pk_bf16_f32 v89, v88, v89
	s_nop 1
	s_nop 0
	v_cndmask_b32_e64 v82, 0, v90, s[38:39]
	v_cndmask_b32_e64 v83, 0, v91, s[38:39]
	v_cndmask_b32_e64 v84, 0, v92, s[38:39]
	v_cndmask_b32_e64 v85, 0, v89, s[38:39]
	v_cndmask_b32_e64 v86, v90, 0, s[38:39]
	v_cndmask_b32_e64 v87, v91, 0, s[38:39]
	v_cndmask_b32_e64 v88, v92, 0, s[38:39]
	v_cndmask_b32_e64 v89, v89, 0, s[38:39]
	s_nop 1
	v_mfma_f32_32x32x16_bf16 v[66:81], v[82:85], v[86:89], v[66:81]
	ds_read_b128 v[82:85], v185 offset:192
	ds_read_b128 v[86:89], v185 offset:208
	ds_read_b128 v[90:93], v186 offset:192
	ds_read_b128 v[94:97], v186 offset:208
	ds_read_b128 v[164:167], v187 offset:4272
	ds_read_b128 v[220:223], v187 offset:4288
	s_waitcnt lgkmcnt(1)
	v_sub_f32_e32 v90, v90, v164
	v_cndmask_b32_e64 v90, v90, -v90, s[38:39]
	v_exp_f32_e32 v90, v90
	s_waitcnt lgkmcnt(0)
	v_sub_f32_e32 v94, v94, v220
	v_mul_f32_e32 v82, v82, v90
	v_cndmask_b32_e64 v90, v94, -v94, s[38:39]
	v_exp_f32_e32 v90, v90
	s_nop 0
	v_mul_f32_e32 v86, v86, v90
	v_sub_f32_e32 v90, v91, v165
	v_cndmask_b32_e64 v90, v90, -v90, s[38:39]
	v_exp_f32_e32 v90, v90
	v_sub_f32_e32 v91, v95, v221
	v_mul_f32_e32 v83, v83, v90
	v_cndmask_b32_e64 v90, v91, -v91, s[38:39]
	v_exp_f32_e32 v90, v90
	v_sub_f32_e32 v91, v96, v222
	v_mul_f32_e32 v87, v87, v90
	v_sub_f32_e32 v90, v92, v166
	v_cndmask_b32_e64 v90, v90, -v90, s[38:39]
	v_exp_f32_e32 v90, v90
	s_nop 0
	v_mul_f32_e32 v84, v84, v90
	v_cndmask_b32_e64 v90, v91, -v91, s[38:39]
	v_exp_f32_e32 v90, v90
	v_sub_f32_e32 v91, v97, v223
	v_mul_f32_e32 v88, v88, v90
	v_sub_f32_e32 v90, v93, v167
	v_cndmask_b32_e64 v90, v90, -v90, s[38:39]
	v_exp_f32_e32 v90, v90
	s_nop 0
	v_mul_f32_e32 v85, v85, v90
	v_cndmask_b32_e64 v90, v91, -v91, s[38:39]
	v_exp_f32_e32 v90, v90
	s_nop 0
	v_mul_f32_e32 v89, v89, v90
	v_cvt_pk_bf16_f32 v90, v82, v83
	s_nop 1
	v_cvt_pk_bf16_f32 v91, v84, v85
	s_nop 1
	v_cvt_pk_bf16_f32 v92, v86, v87
	s_nop 1
	v_cvt_pk_bf16_f32 v89, v88, v89
	s_nop 1
	s_nop 0
	v_cndmask_b32_e64 v82, 0, v90, s[38:39]
	v_cndmask_b32_e64 v83, 0, v91, s[38:39]
	v_cndmask_b32_e64 v84, 0, v92, s[38:39]
	v_cndmask_b32_e64 v85, 0, v89, s[38:39]
	v_cndmask_b32_e64 v86, v90, 0, s[38:39]
	v_cndmask_b32_e64 v87, v91, 0, s[38:39]
	v_cndmask_b32_e64 v88, v92, 0, s[38:39]
	v_cndmask_b32_e64 v89, v89, 0, s[38:39]
	s_nop 1
	v_mfma_f32_32x32x16_bf16 v[66:81], v[82:85], v[86:89], v[66:81]
	s_nop 11
	v_cvt_pk_bf16_f32 v164, v66, v67
	v_cvt_pk_bf16_f32 v165, v68, v69
	v_cvt_pk_bf16_f32 v166, v70, v71
	v_cvt_pk_bf16_f32 v167, v72, v73
	ds_read_b128 v[66:69], v199 offset:17408
	ds_read_b128 v[70:73], v199 offset:17440
	ds_read_b128 v[74:77], v199
	ds_read_b128 v[78:81], v199 offset:32
	s_waitcnt lgkmcnt(1)
	v_exp_f32_e32 v74, v74
	s_nop 0
	v_mul_f32_e32 v66, v66, v74
	s_waitcnt lgkmcnt(0)
	v_exp_f32_e32 v74, v78
	s_nop 0
	v_mul_f32_e32 v70, v70, v74
	v_exp_f32_e32 v74, v75
	s_nop 0
	v_mul_f32_e32 v67, v67, v74
	v_exp_f32_e32 v74, v79
	v_cvt_pk_bf16_f32 v82, v66, v67
	s_nop 1
	s_nop 0
	v_mul_f32_e32 v71, v71, v74
	v_exp_f32_e32 v74, v76
	s_nop 0
	v_mul_f32_e32 v68, v68, v74
	v_exp_f32_e32 v74, v80
	s_nop 0
	v_mul_f32_e32 v72, v72, v74
	v_exp_f32_e32 v74, v77
	s_nop 0
	v_mul_f32_e32 v69, v69, v74
	v_exp_f32_e32 v74, v81
	v_cvt_pk_bf16_f32 v83, v68, v69
	s_nop 1
	v_cvt_pk_bf16_f32 v84, v70, v71
	s_nop 1
	s_nop 0
	v_mul_f32_e32 v73, v73, v74
	v_cvt_pk_bf16_f32 v85, v72, v73
	s_nop 1
	v_cvt_pk_bf16_f32 v66, v2, v3
	s_nop 1
	v_cvt_pk_bf16_f32 v67, v4, v5
	s_nop 1
	v_cvt_pk_bf16_f32 v68, v6, v7
	s_nop 1
	v_cvt_pk_bf16_f32 v69, v8, v9
	s_nop 1
	v_cvt_pk_bf16_f32 v86, v18, v19
	s_nop 1
	v_cvt_pk_bf16_f32 v87, v20, v21
	s_nop 1
	v_cvt_pk_bf16_f32 v88, v22, v23
	s_nop 1
	v_cvt_pk_bf16_f32 v89, v24, v25
	s_nop 1
	ds_read_b128 v[220:223], v199 offset:17472
	ds_read_b128 v[234:237], v199 offset:17504
	ds_read_b128 v[238:241], v199 offset:64
	ds_read_b128 v[242:245], v199 offset:96
	v_mfma_f32_32x32x16_bf16 v[66:81], v[82:85], v[66:69], 0
	s_waitcnt lgkmcnt(1)
	v_exp_f32_e32 v227, v238
	v_exp_f32_e32 v229, v239
	v_exp_f32_e32 v230, v240
	v_exp_f32_e32 v231, v241
	v_mul_f32_e32 v220, v220, v227
	v_mfma_f32_32x32x16_bf16 v[82:97], v[82:85], v[86:89], 0
	s_waitcnt lgkmcnt(0)
	v_exp_f32_e32 v227, v242
	v_mul_f32_e32 v221, v221, v229
	v_exp_f32_e32 v229, v243
	v_mul_f32_e32 v222, v222, v230
	v_exp_f32_e32 v230, v244
	v_mul_f32_e32 v223, v223, v231
	v_exp_f32_e32 v231, v245
	v_mul_f32_e32 v227, v234, v227
	v_mul_f32_e32 v229, v235, v229
	v_mul_f32_e32 v230, v236, v230
	v_mul_f32_e32 v231, v237, v231
	v_cvt_pk_bf16_f32 v220, v220, v221
	s_nop 1
	v_cvt_pk_bf16_f32 v221, v222, v223
	s_nop 1
	v_cvt_pk_bf16_f32 v222, v227, v229
	s_nop 1
	v_cvt_pk_bf16_f32 v223, v230, v231
	s_nop 1
	v_cvt_pk_bf16_f32 v234, v10, v11
	s_nop 1
	v_cvt_pk_bf16_f32 v235, v12, v13
	s_nop 1
	v_cvt_pk_bf16_f32 v236, v14, v15
	s_nop 1
	v_cvt_pk_bf16_f32 v237, v16, v17
	s_nop 1
	s_nop 0
	v_mfma_f32_32x32x16_bf16 v[66:81], v[220:223], v[234:237], v[66:81]
	v_cvt_pk_bf16_f32 v234, v26, v27
	s_nop 1
	v_cvt_pk_bf16_f32 v235, v28, v29
	s_nop 1
	v_cvt_pk_bf16_f32 v236, v30, v31
	s_nop 1
	v_cvt_pk_bf16_f32 v237, v32, v33
	s_nop 1
	s_nop 0
	v_mfma_f32_32x32x16_bf16 v[82:97], v[220:223], v[234:237], v[82:97]
	ds_read_b128 v[220:223], v199 offset:17536
	ds_read_b128 v[234:237], v199 offset:17568
	ds_read_b128 v[238:241], v199 offset:128
	ds_read_b128 v[242:245], v199 offset:160
	s_waitcnt lgkmcnt(1)
	v_exp_f32_e32 v227, v238
	v_exp_f32_e32 v229, v239
	v_exp_f32_e32 v230, v240
	v_exp_f32_e32 v231, v241
	v_mul_f32_e32 v220, v220, v227
	s_waitcnt lgkmcnt(0)
	v_exp_f32_e32 v227, v242
	v_mul_f32_e32 v221, v221, v229
	v_exp_f32_e32 v229, v243
	v_mul_f32_e32 v222, v222, v230
	v_exp_f32_e32 v230, v244
	v_mul_f32_e32 v223, v223, v231
	v_exp_f32_e32 v231, v245
	v_mul_f32_e32 v227, v234, v227
	v_mul_f32_e32 v229, v235, v229
	v_mul_f32_e32 v230, v236, v230
	v_mul_f32_e32 v231, v237, v231
	v_cvt_pk_bf16_f32 v220, v220, v221
	s_nop 1
	v_cvt_pk_bf16_f32 v221, v222, v223
	s_nop 1
	v_cvt_pk_bf16_f32 v222, v227, v229
	s_nop 1
	v_cvt_pk_bf16_f32 v223, v230, v231
	s_nop 1
	v_cvt_pk_bf16_f32 v234, v34, v35
	s_nop 1
	v_cvt_pk_bf16_f32 v235, v36, v37
	s_nop 1
	v_cvt_pk_bf16_f32 v236, v38, v39
	s_nop 1
	v_cvt_pk_bf16_f32 v237, v40, v41
	s_nop 1
	s_nop 0
	v_mfma_f32_32x32x16_bf16 v[66:81], v[220:223], v[234:237], v[66:81]
	v_cvt_pk_bf16_f32 v234, v50, v51
	s_nop 1
	v_cvt_pk_bf16_f32 v235, v52, v53
	s_nop 1
	v_cvt_pk_bf16_f32 v236, v54, v55
	s_nop 1
	v_cvt_pk_bf16_f32 v237, v56, v57
	s_nop 1
	s_nop 0
	v_mfma_f32_32x32x16_bf16 v[82:97], v[220:223], v[234:237], v[82:97]
	ds_read_b128 v[220:223], v199 offset:17600
	ds_read_b128 v[234:237], v199 offset:17632
	ds_read_b128 v[238:241], v199 offset:192
	ds_read_b128 v[242:245], v199 offset:224
	s_waitcnt lgkmcnt(1)
	v_exp_f32_e32 v227, v238
	v_exp_f32_e32 v229, v239
	v_exp_f32_e32 v230, v240
	v_exp_f32_e32 v231, v241
	v_mul_f32_e32 v220, v220, v227
	s_waitcnt lgkmcnt(0)
	v_exp_f32_e32 v227, v242
	v_mul_f32_e32 v221, v221, v229
	v_exp_f32_e32 v229, v243
	v_mul_f32_e32 v222, v222, v230
	v_exp_f32_e32 v230, v244
	v_mul_f32_e32 v223, v223, v231
	v_exp_f32_e32 v231, v245
	v_mul_f32_e32 v227, v234, v227
	v_mul_f32_e32 v229, v235, v229
	v_mul_f32_e32 v230, v236, v230
	v_mul_f32_e32 v231, v237, v231
	v_cvt_pk_bf16_f32 v220, v220, v221
	s_nop 1
	v_cvt_pk_bf16_f32 v221, v222, v223
	s_nop 1
	v_cvt_pk_bf16_f32 v222, v227, v229
	s_nop 1
	v_cvt_pk_bf16_f32 v223, v230, v231
	s_nop 1
	v_cvt_pk_bf16_f32 v234, v42, v43
	s_nop 1
	v_cvt_pk_bf16_f32 v235, v44, v45
	s_nop 1
	v_cvt_pk_bf16_f32 v236, v46, v47
	s_nop 1
	v_cvt_pk_bf16_f32 v237, v48, v49
	s_nop 1
	v_add_u32_e32 v227, 0x6000, v188
	v_mfma_f32_32x32x16_bf16 v[66:81], v[220:223], v[234:237], v[66:81]
	v_cvt_pk_bf16_f32 v234, v58, v59
	s_nop 1
	v_cvt_pk_bf16_f32 v235, v60, v61
	s_nop 1
	v_cvt_pk_bf16_f32 v236, v62, v63
	s_nop 1
	v_cvt_pk_bf16_f32 v237, v64, v65
	s_nop 1
	s_nop 0
	v_mfma_f32_32x32x16_bf16 v[82:97], v[220:223], v[234:237], v[82:97]
	v_cndmask_b32_e64 v220, 0, v216, s[38:39]
	v_cndmask_b32_e64 v221, 0, v217, s[38:39]
	v_cndmask_b32_e64 v222, 0, v218, s[38:39]
	v_cndmask_b32_e64 v223, 0, v219, s[38:39]
	v_cndmask_b32_e64 v216, v216, 0, s[38:39]
	v_cndmask_b32_e64 v217, v217, 0, s[38:39]
	v_cndmask_b32_e64 v218, v218, 0, s[38:39]
	v_mfma_f32_32x32x16_bf16 v[66:81], v[220:223], v[156:159], v[66:81]
	v_cndmask_b32_e64 v219, v219, 0, s[38:39]
	ds_read2_b64 v[234:237], v227 offset0:192 offset1:194
	v_mfma_f32_32x32x16_bf16 v[82:97], v[220:223], v[160:163], v[82:97]
	v_mfma_f32_32x32x16_bf16 v[66:81], v[216:219], v[148:151], v[66:81]
	v_mfma_f32_32x32x16_bf16 v[82:97], v[216:219], v[152:155], v[82:97]
	ds_read2_b64 v[216:219], v200 offset0:192 offset1:194
	s_waitcnt lgkmcnt(1)
	v_mfma_f32_32x32x16_bf16 v[66:81], v[164:167], v[234:237], v[66:81]
	s_waitcnt lgkmcnt(0)
	v_mfma_f32_32x32x16_bf16 v[82:97], v[164:167], v[216:219], v[82:97]
	ds_read_b128 v[164:167], v180 offset:31232
	ds_read_b128 v[216:219], v180 offset:31264
	ds_read_b128 v[220:223], v180 offset:31296
	ds_read_b128 v[234:237], v180 offset:31328
	s_waitcnt lgkmcnt(3)
	v_pk_mul_f32 v[4:5], v[4:5], v[166:167]
	v_pk_mul_f32 v[2:3], v[2:3], v[164:165]
	v_pk_mul_f32 v[20:21], v[20:21], v[166:167]
	v_pk_mul_f32 v[18:19], v[18:19], v[164:165]
	ds_read_b32 v164, v189 offset:31488
	ds_read2st64_b32 v[166:167], v190 offset1:34
	s_waitcnt lgkmcnt(4)
	v_pk_mul_f32 v[6:7], v[6:7], v[216:217]
	v_pk_mul_f32 v[22:23], v[22:23], v[216:217]
	v_pk_mul_f32 v[8:9], v[8:9], v[218:219]
	v_pk_mul_f32 v[24:25], v[24:25], v[218:219]
	s_waitcnt lgkmcnt(0)
	v_sub_f32_e32 v165, v164, v166
	v_exp_f32_e32 v165, v165
	v_add_u32_e32 v166, 0x2200, v191
	v_pk_mul_f32 v[10:11], v[10:11], v[220:221]
	v_pk_mul_f32 v[26:27], v[26:27], v[220:221]
	v_mul_f32_e32 v165, v167, v165
	ds_read2_b32 v[166:167], v166 offset0:68 offset1:136
	ds_read2_b32 v[216:217], v191 offset0:68 offset1:136
	v_pk_mul_f32 v[12:13], v[12:13], v[222:223]
	v_pk_mul_f32 v[28:29], v[28:29], v[222:223]
	v_pk_mul_f32 v[16:17], v[16:17], v[236:237]
	v_pk_mul_f32 v[14:15], v[14:15], v[234:235]
	s_waitcnt lgkmcnt(0)
	v_sub_f32_e32 v216, v164, v216
	v_exp_f32_e32 v216, v216
	v_pk_mul_f32 v[32:33], v[32:33], v[236:237]
	v_pk_mul_f32 v[30:31], v[30:31], v[234:235]
	v_mul_f32_e32 v218, v166, v216
	v_sub_f32_e32 v166, v164, v217
	v_add_u32_e32 v216, 0x200, v191
	v_exp_f32_e32 v166, v166
	ds_read2_b32 v[216:217], v216 offset0:76 offset1:144
	v_mul_f32_e32 v219, v167, v166
	v_add_u32_e32 v166, 0x2400, v191
	ds_read2_b32 v[166:167], v166 offset0:76 offset1:144
	s_waitcnt lgkmcnt(1)
	v_sub_f32_e32 v216, v164, v216
	v_exp_f32_e32 v216, v216
	s_waitcnt lgkmcnt(0)
	v_mul_f32_e32 v220, v166, v216
	v_sub_f32_e32 v166, v164, v217
	v_add_u32_e32 v216, 0x400, v191
	v_exp_f32_e32 v166, v166
	ds_read2_b32 v[216:217], v216 offset0:84 offset1:152
	v_mul_f32_e32 v221, v167, v166
	v_add_u32_e32 v166, 0x2600, v191
	ds_read2_b32 v[166:167], v166 offset0:84 offset1:152
	s_waitcnt lgkmcnt(1)
	v_sub_f32_e32 v216, v164, v216
	v_exp_f32_e32 v216, v216
	s_waitcnt lgkmcnt(0)
	v_mul_f32_e32 v166, v166, v216
	v_sub_f32_e32 v216, v164, v217
	v_exp_f32_e32 v216, v216
	s_nop 0
	v_mul_f32_e32 v167, v167, v216
	ds_read_b32 v216, v191 offset:10608
	ds_read_b32 v217, v191 offset:1904
	s_waitcnt lgkmcnt(0)
	v_sub_f32_e32 v217, v164, v217
	v_exp_f32_e32 v217, v217
	s_nop 0
	v_mul_f32_e32 v222, v216, v217
	v_cvt_pk_bf16_f32 v216, v165, v218
	s_nop 1
	v_cvt_pk_bf16_f32 v217, v219, v220
	s_nop 1
	v_cvt_pk_bf16_f32 v218, v221, v166
	s_nop 1
	v_cvt_pk_bf16_f32 v219, v167, v222
	s_nop 1
	ds_read2st64_b32 v[166:167], v192 offset1:34
	v_mfma_f32_32x32x16_bf16 v[2:17], v[216:219], v[156:159], v[2:17]
	s_waitcnt lgkmcnt(0)
	v_sub_f32_e32 v165, v164, v166
	v_exp_f32_e32 v165, v165
	s_nop 0
	v_mul_f32_e32 v165, v167, v165
	v_mfma_f32_32x32x16_bf16 v[18:33], v[216:219], v[160:163], v[18:33]
	v_add_u32_e32 v216, 0x1000, v191
	ds_read2_b32 v[216:217], v216 offset0:132 offset1:200
	v_add_u32_e32 v218, 0x3400, v191
	ds_read2_b32 v[166:167], v218 offset0:4 offset1:72
	s_waitcnt lgkmcnt(1)
	v_sub_f32_e32 v216, v164, v216
	v_exp_f32_e32 v216, v216
	s_waitcnt lgkmcnt(0)
	v_mul_f32_e32 v219, v166, v216
	v_sub_f32_e32 v166, v164, v217
	v_exp_f32_e32 v166, v166
	s_nop 0
	v_mul_f32_e32 v220, v167, v166
	ds_read2_b32 v[166:167], v218 offset0:140 offset1:208
	v_add_u32_e32 v218, 0x1400, v191
	ds_read2_b32 v[216:217], v218 offset0:12 offset1:80
	s_waitcnt lgkmcnt(0)
	v_sub_f32_e32 v216, v164, v216
	v_exp_f32_e32 v216, v216
	s_nop 0
	v_mul_f32_e32 v221, v166, v216
	v_sub_f32_e32 v166, v164, v217
	v_exp_f32_e32 v166, v166
	s_nop 0
	v_mul_f32_e32 v222, v167, v166
	v_add_u32_e32 v166, 0x3800, v191
	ds_read2_b32 v[166:167], v166 offset0:20 offset1:88
	ds_read2_b32 v[216:217], v218 offset0:148 offset1:216
	s_waitcnt lgkmcnt(0)
	v_sub_f32_e32 v216, v164, v216
	v_exp_f32_e32 v216, v216
	s_nop 0
	v_mul_f32_e32 v166, v166, v216
	v_sub_f32_e32 v216, v164, v217
	v_exp_f32_e32 v216, v216
	s_nop 0
	v_mul_f32_e32 v167, v167, v216
	ds_read_b32 v216, v191 offset:14960
	ds_read_b32 v217, v191 offset:6256
	s_waitcnt lgkmcnt(0)
	v_sub_f32_e32 v164, v164, v217
	v_exp_f32_e32 v164, v164
	s_nop 0
	v_mul_f32_e32 v216, v216, v164
	v_cvt_pk_bf16_f32 v164, v165, v219
	s_nop 1
	v_cvt_pk_bf16_f32 v165, v220, v221
	s_nop 1
	v_cvt_pk_bf16_f32 v166, v222, v166
	s_nop 1
	v_cvt_pk_bf16_f32 v167, v167, v216
	s_nop 1
	s_nop 0
	v_mfma_f32_32x32x16_bf16 v[2:17], v[164:167], v[148:151], v[2:17]
	v_mfma_f32_32x32x16_bf16 v[18:33], v[164:167], v[152:155], v[18:33]
	ds_read_b128 v[164:167], v180 offset:31360
	ds_read_b128 v[216:219], v180 offset:31392
	ds_read_b128 v[220:223], v180 offset:31424
	ds_read_b128 v[234:237], v180 offset:31456
	s_waitcnt lgkmcnt(3)
	v_pk_mul_f32 v[34:35], v[34:35], v[164:165]
	v_pk_mul_f32 v[50:51], v[50:51], v[164:165]
	v_add_u32_e32 v164, 0x80, v191
	s_waitcnt lgkmcnt(2)
	v_pk_mul_f32 v[38:39], v[38:39], v[216:217]
	v_pk_mul_f32 v[54:55], v[54:55], v[216:217]
	ds_read_b32 v216, v172 offset:31616
	ds_read2st64_b32 v[164:165], v164 offset1:34
	v_pk_mul_f32 v[36:37], v[36:37], v[166:167]
	v_pk_mul_f32 v[52:53], v[52:53], v[166:167]
	v_pk_mul_f32 v[40:41], v[40:41], v[218:219]
	v_pk_mul_f32 v[56:57], v[56:57], v[218:219]
	s_waitcnt lgkmcnt(0)
	v_sub_f32_e32 v164, v216, v164
	v_exp_f32_e32 v164, v164
	v_pk_mul_f32 v[42:43], v[42:43], v[220:221]
	v_pk_mul_f32 v[58:59], v[58:59], v[220:221]
	v_pk_mul_f32 v[48:49], v[48:49], v[236:237]
	v_mul_f32_e32 v217, v165, v164
	v_add_u32_e32 v164, 0x2200, v193
	ds_read2_b32 v[164:165], v164 offset0:68 offset1:136
	ds_read2_b32 v[166:167], v193 offset0:68 offset1:136
	v_pk_mul_f32 v[44:45], v[44:45], v[222:223]
	v_pk_mul_f32 v[46:47], v[46:47], v[234:235]
	v_pk_mul_f32 v[60:61], v[60:61], v[222:223]
	v_pk_mul_f32 v[64:65], v[64:65], v[236:237]
	s_waitcnt lgkmcnt(0)
	v_sub_f32_e32 v166, v216, v166
	v_exp_f32_e32 v166, v166
	v_pk_mul_f32 v[62:63], v[62:63], v[234:235]
	v_mul_f32_e32 v218, v164, v166
	v_sub_f32_e32 v164, v216, v167
	v_add_u32_e32 v166, 0x200, v193
	v_exp_f32_e32 v164, v164
	ds_read2_b32 v[166:167], v166 offset0:76 offset1:144
	v_mul_f32_e32 v219, v165, v164
	v_add_u32_e32 v164, 0x2400, v193
	ds_read2_b32 v[164:165], v164 offset0:76 offset1:144
	s_waitcnt lgkmcnt(1)
	v_sub_f32_e32 v166, v216, v166
	v_exp_f32_e32 v166, v166
	s_waitcnt lgkmcnt(0)
	v_mul_f32_e32 v220, v164, v166
	v_sub_f32_e32 v164, v216, v167
	v_add_u32_e32 v166, 0x400, v193
	v_exp_f32_e32 v164, v164
	ds_read2_b32 v[166:167], v166 offset0:84 offset1:152
	v_mul_f32_e32 v221, v165, v164
	v_add_u32_e32 v164, 0x2600, v193
	ds_read2_b32 v[164:165], v164 offset0:84 offset1:152
	s_waitcnt lgkmcnt(1)
	v_sub_f32_e32 v166, v216, v166
	v_exp_f32_e32 v166, v166
	s_waitcnt lgkmcnt(0)
	v_mul_f32_e32 v166, v164, v166
	v_sub_f32_e32 v164, v216, v167
	v_exp_f32_e32 v164, v164
	s_nop 0
	v_mul_f32_e32 v167, v165, v164
	ds_read_b32 v164, v193 offset:10608
	ds_read_b32 v165, v193 offset:1904
	s_waitcnt lgkmcnt(0)
	v_sub_f32_e32 v165, v216, v165
	v_exp_f32_e32 v165, v165
	s_nop 0
	v_mul_f32_e32 v222, v164, v165
	v_cvt_pk_bf16_f32 v164, v217, v218
	s_nop 1
	v_cvt_pk_bf16_f32 v165, v219, v220
	s_nop 1
	v_cvt_pk_bf16_f32 v166, v221, v166
	s_nop 1
	v_cvt_pk_bf16_f32 v167, v167, v222
	s_nop 1
	s_nop 0
	v_mfma_f32_32x32x16_bf16 v[34:49], v[164:167], v[156:159], v[34:49]
	ds_read2st64_b32 v[156:157], v201 offset1:34
	v_add_u32_e32 v158, 0x1000, v193
	ds_read2_b32 v[158:159], v158 offset0:132 offset1:200
	s_waitcnt lgkmcnt(1)
	v_sub_f32_e32 v156, v216, v156
	v_exp_f32_e32 v156, v156
	v_mfma_f32_32x32x16_bf16 v[50:65], v[164:167], v[160:163], v[50:65]
	v_add_u32_e32 v161, 0x3400, v193
	s_waitcnt lgkmcnt(0)
	v_sub_f32_e32 v158, v216, v158
	v_mul_f32_e32 v160, v157, v156
	ds_read2_b32 v[156:157], v161 offset0:4 offset1:72
	v_exp_f32_e32 v158, v158
	s_waitcnt lgkmcnt(0)
	v_mul_f32_e32 v162, v156, v158
	v_sub_f32_e32 v156, v216, v159
	v_exp_f32_e32 v156, v156
	s_nop 0
	v_mul_f32_e32 v163, v157, v156
	ds_read2_b32 v[156:157], v161 offset0:140 offset1:208
	v_add_u32_e32 v161, 0x1400, v193
	ds_read2_b32 v[158:159], v161 offset0:12 offset1:80
	s_waitcnt lgkmcnt(0)
	v_sub_f32_e32 v158, v216, v158
	v_exp_f32_e32 v158, v158
	s_nop 0
	v_mul_f32_e32 v164, v156, v158
	v_sub_f32_e32 v156, v216, v159
	v_exp_f32_e32 v156, v156
	s_nop 0
	v_mul_f32_e32 v165, v157, v156
	v_add_u32_e32 v156, 0x3800, v193
	ds_read2_b32 v[156:157], v156 offset0:20 offset1:88
	ds_read2_b32 v[158:159], v161 offset0:148 offset1:216
	s_waitcnt lgkmcnt(0)
	v_sub_f32_e32 v158, v216, v158
	v_exp_f32_e32 v158, v158
	s_nop 0
	v_mul_f32_e32 v158, v156, v158
	v_sub_f32_e32 v156, v216, v159
	v_exp_f32_e32 v156, v156
	s_nop 0
	v_mul_f32_e32 v159, v157, v156
	ds_read_b32 v156, v193 offset:14960
	ds_read_b32 v157, v193 offset:6256
	s_waitcnt lgkmcnt(0)
	v_sub_f32_e32 v157, v216, v157
	v_exp_f32_e32 v157, v157
	s_nop 0
	v_mul_f32_e32 v161, v156, v157
	v_cvt_pk_bf16_f32 v156, v160, v162
	s_nop 1
	v_cvt_pk_bf16_f32 v157, v163, v164
	s_nop 1
	v_cvt_pk_bf16_f32 v158, v165, v158
	s_nop 1
	v_cvt_pk_bf16_f32 v159, v159, v161
	s_nop 1
	s_nop 0
	v_mfma_f32_32x32x16_bf16 v[34:49], v[156:159], v[148:151], v[34:49]
	v_add_u32_e32 v148, s1, v177
	v_mad_i64_i32 v[148:149], s[22:23], v148, s96, v[168:169]
	global_load_dwordx4 v[160:163], v[148:149], off offset:2752
	v_add_co_u32_e32 v150, vcc, s33, v148
	s_nop 1
	v_addc_co_u32_e32 v151, vcc, 0, v149, vcc
	v_mfma_f32_32x32x16_bf16 v[50:65], v[156:159], v[152:155], v[50:65]
	global_load_dwordx4 v[156:159], v[150:151], off offset:2752
	v_add_co_u32_e32 v150, vcc, s84, v148
	s_waitcnt vmcnt(1)
	v_lshlrev_b32_e32 v164, 16, v160
	v_addc_co_u32_e32 v151, vcc, 0, v149, vcc
	global_load_dwordx4 v[152:155], v[150:151], off offset:2752
	v_add_co_u32_e32 v148, vcc, s97, v148
	v_and_b32_e32 v165, 0xffff0000, v160
	s_nop 0
	v_addc_co_u32_e32 v149, vcc, 0, v149, vcc
	global_load_dwordx4 v[148:151], v[148:149], off offset:2752
	v_mul_f32_e32 v160, 0xbfb8aa3b, v164
	v_exp_f32_e32 v160, v160
	s_nop 0
	v_add_f32_e32 v160, 1.0, v160
	v_rcp_f32_e32 v166, v160
	v_mul_f32_e32 v160, 0xbfb8aa3b, v165
	v_exp_f32_e32 v160, v160
	s_nop 0
	v_add_f32_e32 v160, 1.0, v160
	v_rcp_f32_e32 v167, v160
	v_lshlrev_b32_e32 v160, 16, v161
	v_and_b32_e32 v161, 0xffff0000, v161
	v_mul_f32_e32 v216, 0xbfb8aa3b, v160
	v_mul_f32_e32 v217, 0xbfb8aa3b, v161
	v_exp_f32_e32 v216, v216
	v_exp_f32_e32 v217, v217
	v_pk_mul_f32 v[164:165], v[166:167], v[164:165]
	v_add_f32_e32 v216, 1.0, v216
	v_add_f32_e32 v217, 1.0, v217
	v_rcp_f32_e32 v216, v216
	v_rcp_f32_e32 v217, v217
	s_nop 0
	v_pk_mul_f32 v[166:167], v[216:217], v[160:161]
	s_waitcnt vmcnt(2)
	v_lshlrev_b32_e32 v160, 16, v156
	v_and_b32_e32 v161, 0xffff0000, v156
	v_mul_f32_e32 v156, 0xbfb8aa3b, v160
	v_exp_f32_e32 v156, v156
	ds_write_b128 v170, v[164:167] offset:17408
	v_add_f32_e32 v156, 1.0, v156
	v_rcp_f32_e32 v164, v156
	v_mul_f32_e32 v156, 0xbfb8aa3b, v161
	v_exp_f32_e32 v156, v156
	s_nop 0
	v_add_f32_e32 v156, 1.0, v156
	v_rcp_f32_e32 v165, v156
	v_lshlrev_b32_e32 v156, 16, v157
	v_and_b32_e32 v157, 0xffff0000, v157
	v_mul_f32_e32 v166, 0xbfb8aa3b, v156
	v_mul_f32_e32 v167, 0xbfb8aa3b, v157
	v_exp_f32_e32 v166, v166
	v_exp_f32_e32 v167, v167
	v_pk_mul_f32 v[164:165], v[164:165], v[160:161]
	v_add_f32_e32 v166, 1.0, v166
	v_add_f32_e32 v167, 1.0, v167
	v_rcp_f32_e32 v166, v166
	v_rcp_f32_e32 v167, v167
	s_nop 0
	v_pk_mul_f32 v[166:167], v[166:167], v[156:157]
	ds_write_b128 v170, v[164:167] offset:19584
	s_waitcnt vmcnt(1)
	v_lshlrev_b32_e32 v156, 16, v152
	v_and_b32_e32 v157, 0xffff0000, v152
	v_mul_f32_e32 v152, 0xbfb8aa3b, v156
	v_exp_f32_e32 v152, v152
	s_nop 0
	v_add_f32_e32 v152, 1.0, v152
	v_rcp_f32_e32 v160, v152
	v_mul_f32_e32 v152, 0xbfb8aa3b, v157
	v_exp_f32_e32 v152, v152
	s_nop 0
	v_add_f32_e32 v152, 1.0, v152
	v_rcp_f32_e32 v161, v152
	v_lshlrev_b32_e32 v152, 16, v153
	v_mul_f32_e32 v164, 0xbfb8aa3b, v152
	v_exp_f32_e32 v164, v164
	v_and_b32_e32 v153, 0xffff0000, v153
	v_add_f32_e32 v164, 1.0, v164
	v_rcp_f32_e32 v166, v164
	v_mul_f32_e32 v164, 0xbfb8aa3b, v153
	v_exp_f32_e32 v164, v164
	s_nop 0
	v_add_f32_e32 v164, 1.0, v164
	v_rcp_f32_e32 v167, v164
	v_pk_mul_f32 v[164:165], v[160:161], v[156:157]
	v_pk_mul_f32 v[166:167], v[166:167], v[152:153]
	s_waitcnt vmcnt(0)
	v_lshlrev_b32_e32 v152, 16, v148
	v_and_b32_e32 v153, 0xffff0000, v148
	v_mul_f32_e32 v148, 0xbfb8aa3b, v152
	v_exp_f32_e32 v148, v148
	ds_write_b128 v170, v[164:167] offset:21760
	v_add_f32_e32 v148, 1.0, v148
	v_rcp_f32_e32 v156, v148
	v_mul_f32_e32 v148, 0xbfb8aa3b, v153
	v_exp_f32_e32 v148, v148
	s_nop 0
	v_add_f32_e32 v148, 1.0, v148
	v_rcp_f32_e32 v157, v148
	v_lshlrev_b32_e32 v148, 16, v149
	v_and_b32_e32 v149, 0xffff0000, v149
	v_mul_f32_e32 v160, 0xbfb8aa3b, v148
	v_mul_f32_e32 v161, 0xbfb8aa3b, v149
	v_exp_f32_e32 v160, v160
	v_exp_f32_e32 v161, v161
	v_pk_mul_f32 v[164:165], v[156:157], v[152:153]
	v_lshlrev_b32_e32 v156, 16, v163
	v_add_f32_e32 v160, 1.0, v160
	v_add_f32_e32 v161, 1.0, v161
	v_rcp_f32_e32 v160, v160
	v_rcp_f32_e32 v161, v161
	v_and_b32_e32 v157, 0xffff0000, v163
	v_pk_mul_f32 v[166:167], v[160:161], v[148:149]
	v_mul_f32_e32 v160, 0xbfb8aa3b, v156
	v_exp_f32_e32 v160, v160
	v_lshlrev_b32_e32 v148, 16, v162
	v_and_b32_e32 v149, 0xffff0000, v162
	v_mul_f32_e32 v152, 0xbfb8aa3b, v148
	v_mul_f32_e32 v153, 0xbfb8aa3b, v149
	v_add_f32_e32 v160, 1.0, v160
	v_exp_f32_e32 v152, v152
	v_exp_f32_e32 v153, v153
	v_rcp_f32_e32 v162, v160
	v_mul_f32_e32 v160, 0xbfb8aa3b, v157
	v_exp_f32_e32 v160, v160
	v_add_f32_e32 v152, 1.0, v152
	v_add_f32_e32 v153, 1.0, v153
	v_rcp_f32_e32 v152, v152
	v_rcp_f32_e32 v153, v153
	v_add_f32_e32 v160, 1.0, v160
	v_rcp_f32_e32 v163, v160
	ds_write_b128 v170, v[164:167] offset:23936
	v_pk_mul_f32 v[160:161], v[152:153], v[148:149]
	v_lshlrev_b32_e32 v148, 16, v158
	v_and_b32_e32 v149, 0xffff0000, v158
	v_lshlrev_b32_e32 v158, 16, v159
	v_pk_mul_f32 v[162:163], v[162:163], v[156:157]
	v_mul_f32_e32 v156, 0xbfb8aa3b, v158
	v_exp_f32_e32 v156, v156
	v_mul_f32_e32 v152, 0xbfb8aa3b, v148
	v_mul_f32_e32 v153, 0xbfb8aa3b, v149
	v_exp_f32_e32 v152, v152
	v_exp_f32_e32 v153, v153
	v_and_b32_e32 v159, 0xffff0000, v159
	v_add_f32_e32 v156, 1.0, v156
	ds_write_b128 v170, v[160:163] offset:17424
	v_rcp_f32_e32 v160, v156
	v_mul_f32_e32 v156, 0xbfb8aa3b, v159
	v_add_f32_e32 v152, 1.0, v152
	v_add_f32_e32 v153, 1.0, v153
	v_exp_f32_e32 v156, v156
	v_rcp_f32_e32 v152, v152
	v_rcp_f32_e32 v153, v153
	v_add_f32_e32 v156, 1.0, v156
	v_rcp_f32_e32 v161, v156
	v_pk_mul_f32 v[156:157], v[152:153], v[148:149]
	v_lshlrev_b32_e32 v148, 16, v154
	v_and_b32_e32 v149, 0xffff0000, v154
	v_mul_f32_e32 v152, 0xbfb8aa3b, v148
	v_mul_f32_e32 v153, 0xbfb8aa3b, v149
	v_exp_f32_e32 v152, v152
	v_exp_f32_e32 v153, v153
	v_pk_mul_f32 v[158:159], v[160:161], v[158:159]
	v_lshlrev_b32_e32 v154, 16, v155
	v_add_f32_e32 v152, 1.0, v152
	v_add_f32_e32 v153, 1.0, v153
	v_and_b32_e32 v155, 0xffff0000, v155
	ds_write_b128 v170, v[156:159] offset:19600
	v_rcp_f32_e32 v152, v152
	v_rcp_f32_e32 v153, v153
	v_mul_f32_e32 v156, 0xbfb8aa3b, v154
	v_mul_f32_e32 v157, 0xbfb8aa3b, v155
	v_exp_f32_e32 v156, v156
	v_exp_f32_e32 v157, v157
	v_pk_mul_f32 v[152:153], v[152:153], v[148:149]
	v_lshlrev_b32_e32 v148, 16, v150
	v_add_f32_e32 v156, 1.0, v156
	v_add_f32_e32 v157, 1.0, v157
	v_and_b32_e32 v149, 0xffff0000, v150
	v_mul_f32_e32 v150, 0xbfb8aa3b, v148
	v_rcp_f32_e32 v156, v156
	v_rcp_f32_e32 v157, v157
	v_exp_f32_e32 v150, v150
	v_pk_mul_f32 v[154:155], v[156:157], v[154:155]
	v_add_f32_e32 v150, 1.0, v150
	ds_write_b128 v170, v[152:155] offset:21776
	v_rcp_f32_e32 v152, v150
	v_mul_f32_e32 v150, 0xbfb8aa3b, v149
	v_exp_f32_e32 v150, v150
	s_nop 0
	v_add_f32_e32 v150, 1.0, v150
	v_rcp_f32_e32 v153, v150
	v_lshlrev_b32_e32 v150, 16, v151
	v_and_b32_e32 v151, 0xffff0000, v151
	v_mul_f32_e32 v154, 0xbfb8aa3b, v150
	v_mul_f32_e32 v155, 0xbfb8aa3b, v151
	v_exp_f32_e32 v154, v154
	v_exp_f32_e32 v155, v155
	v_pk_mul_f32 v[148:149], v[152:153], v[148:149]
	v_add_f32_e32 v154, 1.0, v154
	v_add_f32_e32 v155, 1.0, v155
	v_rcp_f32_e32 v154, v154
	v_rcp_f32_e32 v155, v155
	s_nop 0
	v_pk_mul_f32 v[150:151], v[154:155], v[150:151]
	ds_write_b128 v170, v[148:151] offset:23952
	v_mul_f32_e32 v148, v82, v82
	v_fmac_f32_e32 v148, v66, v66
	v_mov_b32_e32 v149, v115
	ds_read_b32 v152, v194 offset:17408
	ds_read_b32 v155, v195 offset:17536
	v_add_f32_dpp v148, v148, v148 quad_perm:[1,0,3,2] row_mask:0xf bank_mask:0xf bound_ctrl:1
	s_nop 1
	v_add_f32_dpp v148, v148, v148 quad_perm:[2,3,0,1] row_mask:0xf bank_mask:0xf bound_ctrl:1
	s_nop 1
	v_add_f32_dpp v148, v148, v148 row_half_mirror row_mask:0xf bank_mask:0xf bound_ctrl:1
	s_nop 1
	v_add_f32_dpp v148, v148, v148 row_mirror row_mask:0xf bank_mask:0xf bound_ctrl:1
	s_nop 1
	v_mov_b32_dpp v149, v148 row_bcast:15 row_mask:0xa bank_mask:0xf
	v_add_f32_e32 v148, v148, v149
	s_nop 0
	v_readlane_b32 s22, v148, 31
	v_readlane_b32 s23, v148, 63
	s_nop 0
	v_mov_b32_e32 v149, s22
	v_mov_b32_e32 v148, s23
	v_cndmask_b32_e64 v148, v148, v149, s[40:41]
	v_fmamk_f32 v148, v148, 0x3c800000, v225
	v_rsq_f32_e32 v154, v148
	v_add_u32_e32 v148, s1, v183
	v_ashrrev_i32_e32 v149, 31, v148
	v_lshlrev_b64 v[150:151], 11, v[148:149]
	v_lshl_add_u64 v[150:151], s[74:75], 0, v[150:151]
	v_mul_f32_e32 v66, v66, v154
	v_lshl_add_u64 v[150:151], v[150:151], 0, s[80:81]
	v_mul_f32_e32 v66, v173, v66
	s_waitcnt lgkmcnt(1)
	v_mul_f32_e32 v66, v152, v66
	v_lshl_add_u64 v[150:151], v[150:151], 0, v[114:115]
	v_bfe_u32 v149, v66, 16, 1
	v_lshl_add_u64 v[152:153], v[150:151], 0, s[6:7]
	v_add_co_u32_e32 v150, vcc, s83, v150
	v_add3_u32 v66, v66, v149, s9
	s_nop 0
	v_addc_co_u32_e32 v151, vcc, 0, v151, vcc
	global_store_short_d16_hi v[150:151], v66, off offset:1024
	v_mul_f32_e32 v66, v82, v154
	v_mul_f32_e32 v66, v176, v66
	s_waitcnt lgkmcnt(0)
	v_mul_f32_e32 v66, v155, v66
	v_bfe_u32 v82, v66, 16, 1
	v_add3_u32 v66, v66, v82, s9
	global_store_short_d16_hi v[152:153], v66, off offset:64
	v_mul_f32_e32 v66, v83, v83
	v_fmac_f32_e32 v66, v67, v67
	v_mov_b32_e32 v82, v115
	v_add_u32_e32 v150, s1, v196
	v_add_f32_dpp v66, v66, v66 quad_perm:[1,0,3,2] row_mask:0xf bank_mask:0xf bound_ctrl:1
	v_ashrrev_i32_e32 v151, 31, v150
	v_lshlrev_b64 v[150:151], 11, v[150:151]
	v_add_f32_dpp v66, v66, v66 quad_perm:[2,3,0,1] row_mask:0xf bank_mask:0xf bound_ctrl:1
	v_lshl_add_u64 v[150:151], s[74:75], 0, v[150:151]
	v_lshl_add_u64 v[150:151], v[150:151], 0, s[80:81]
	v_add_f32_dpp v66, v66, v66 row_half_mirror row_mask:0xf bank_mask:0xf bound_ctrl:1
	s_nop 1
	v_add_f32_dpp v66, v66, v66 row_mirror row_mask:0xf bank_mask:0xf bound_ctrl:1
	s_nop 1
	v_mov_b32_dpp v82, v66 row_bcast:15 row_mask:0xa bank_mask:0xf
	v_add_f32_e32 v66, v66, v82
	s_nop 0
	v_readlane_b32 s22, v66, 31
	v_readlane_b32 s23, v66, 63
	s_nop 0
	v_mov_b32_e32 v82, s22
	v_mov_b32_e32 v66, s23
	v_cndmask_b32_e64 v66, v66, v82, s[40:41]
	v_fmamk_f32 v66, v66, 0x3c800000, v225
	v_rsq_f32_e32 v82, v66
	v_add_u32_e32 v66, 0x4400, v174
	ds_read2_b32 v[152:153], v66 offset1:32
	v_mul_f32_e32 v66, v67, v82
	v_mul_f32_e32 v66, v173, v66
	s_waitcnt lgkmcnt(0)
	v_mul_f32_e32 v66, v152, v66
	v_bfe_u32 v67, v66, 16, 1
	v_add3_u32 v149, v66, v67, s9
	v_lshl_add_u64 v[66:67], v[150:151], 0, v[114:115]
	v_lshl_add_u64 v[150:151], v[66:67], 0, s[6:7]
	v_add_co_u32_e32 v66, vcc, s83, v66
	s_nop 1
	v_addc_co_u32_e32 v67, vcc, 0, v67, vcc
	global_store_short_d16_hi v[66:67], v149, off offset:1024
	v_mul_f32_e32 v66, v83, v82
	v_mul_f32_e32 v66, v176, v66
	v_mul_f32_e32 v66, v153, v66
	v_bfe_u32 v67, v66, 16, 1
	v_add3_u32 v66, v66, v67, s9
	global_store_short_d16_hi v[150:151], v66, off offset:64
	v_mul_f32_e32 v66, v84, v84
	v_fmac_f32_e32 v66, v68, v68
	v_mov_b32_e32 v67, v115
	ds_read2_b32 v[82:83], v202 offset1:32
	v_add_f32_dpp v66, v66, v66 quad_perm:[1,0,3,2] row_mask:0xf bank_mask:0xf bound_ctrl:1
	s_nop 1
	v_add_f32_dpp v66, v66, v66 quad_perm:[2,3,0,1] row_mask:0xf bank_mask:0xf bound_ctrl:1
	s_nop 1
	v_add_f32_dpp v66, v66, v66 row_half_mirror row_mask:0xf bank_mask:0xf bound_ctrl:1
	s_nop 1
	v_add_f32_dpp v66, v66, v66 row_mirror row_mask:0xf bank_mask:0xf bound_ctrl:1
	s_nop 1
	v_mov_b32_dpp v67, v66 row_bcast:15 row_mask:0xa bank_mask:0xf
	v_add_f32_e32 v66, v66, v67
	s_nop 0
	v_readlane_b32 s22, v66, 31
	v_readlane_b32 s23, v66, 63
	s_nop 0
	v_mov_b32_e32 v67, s22
	v_mov_b32_e32 v66, s23
	v_cndmask_b32_e64 v66, v66, v67, s[40:41]
	v_fmamk_f32 v66, v66, 0x3c800000, v225
	v_rsq_f32_e32 v149, v66
	v_add_u32_e32 v66, s1, v175
	v_ashrrev_i32_e32 v67, 31, v66
	v_lshlrev_b64 v[66:67], 11, v[66:67]
	v_lshl_add_u64 v[66:67], s[74:75], 0, v[66:67]
	v_mul_f32_e32 v68, v68, v149
	v_lshl_add_u64 v[66:67], v[66:67], 0, s[80:81]
	v_mul_f32_e32 v68, v173, v68
	s_waitcnt lgkmcnt(0)
	v_mul_f32_e32 v68, v82, v68
	v_lshl_add_u64 v[66:67], v[66:67], 0, v[114:115]
	v_bfe_u32 v82, v68, 16, 1
	v_lshl_add_u64 v[150:151], v[66:67], 0, s[6:7]
	v_add_co_u32_e32 v66, vcc, s83, v66
	v_add3_u32 v68, v68, v82, s9
	s_nop 0
	v_addc_co_u32_e32 v67, vcc, 0, v67, vcc
	global_store_short_d16_hi v[66:67], v68, off offset:1024
	v_mul_f32_e32 v66, v84, v149
	v_mul_f32_e32 v66, v176, v66
	v_mul_f32_e32 v66, v83, v66
	v_bfe_u32 v67, v66, 16, 1
	v_add3_u32 v66, v66, v67, s9
	global_store_short_d16_hi v[150:151], v66, off offset:64
	v_mul_f32_e32 v66, v85, v85
	v_fmac_f32_e32 v66, v69, v69
	v_mov_b32_e32 v67, v115
	ds_read2_b32 v[82:83], v203 offset1:32
	v_add_f32_dpp v66, v66, v66 quad_perm:[1,0,3,2] row_mask:0xf bank_mask:0xf bound_ctrl:1
	s_nop 1
	v_add_f32_dpp v66, v66, v66 quad_perm:[2,3,0,1] row_mask:0xf bank_mask:0xf bound_ctrl:1
	s_nop 1
	v_add_f32_dpp v66, v66, v66 row_half_mirror row_mask:0xf bank_mask:0xf bound_ctrl:1
	s_nop 1
	v_add_f32_dpp v66, v66, v66 row_mirror row_mask:0xf bank_mask:0xf bound_ctrl:1
	s_nop 1
	v_mov_b32_dpp v67, v66 row_bcast:15 row_mask:0xa bank_mask:0xf
	v_add_f32_e32 v66, v66, v67
	s_nop 0
	v_readlane_b32 s22, v66, 31
	v_readlane_b32 s23, v66, 63
	s_nop 0
	v_mov_b32_e32 v67, s22
	v_mov_b32_e32 v66, s23
	v_cndmask_b32_e64 v66, v66, v67, s[40:41]
	v_fmamk_f32 v66, v66, 0x3c800000, v225
	v_rsq_f32_e32 v84, v66
	v_add_u32_e32 v66, s1, v197
	v_ashrrev_i32_e32 v67, 31, v66
	v_lshlrev_b64 v[66:67], 11, v[66:67]
	v_mul_f32_e32 v68, v69, v84
	v_lshl_add_u64 v[66:67], s[74:75], 0, v[66:67]
	v_mul_f32_e32 v68, v173, v68
	v_lshl_add_u64 v[66:67], v[66:67], 0, s[80:81]
	s_waitcnt lgkmcnt(0)
	v_mul_f32_e32 v68, v82, v68
	v_bfe_u32 v69, v68, 16, 1
	v_lshl_add_u64 v[66:67], v[66:67], 0, v[114:115]
	v_add3_u32 v82, v68, v69, s9
	v_lshl_add_u64 v[68:69], v[66:67], 0, s[6:7]
	v_add_co_u32_e32 v66, vcc, s83, v66
	s_nop 1
	v_addc_co_u32_e32 v67, vcc, 0, v67, vcc
	global_store_short_d16_hi v[66:67], v82, off offset:1024
	v_mul_f32_e32 v66, v85, v84
	v_mul_f32_e32 v66, v176, v66
	v_mul_f32_e32 v66, v83, v66
	v_bfe_u32 v67, v66, 16, 1
	v_add3_u32 v66, v66, v67, s9
	global_store_short_d16_hi v[68:69], v66, off offset:64
	v_mul_f32_e32 v66, v86, v86
	v_fmac_f32_e32 v66, v70, v70
	v_mov_b32_e32 v67, v115
	ds_read2_b32 v[68:69], v204 offset1:32
	v_add_f32_dpp v66, v66, v66 quad_perm:[1,0,3,2] row_mask:0xf bank_mask:0xf bound_ctrl:1
	s_nop 1
	v_add_f32_dpp v66, v66, v66 quad_perm:[2,3,0,1] row_mask:0xf bank_mask:0xf bound_ctrl:1
	s_nop 1
	v_add_f32_dpp v66, v66, v66 row_half_mirror row_mask:0xf bank_mask:0xf bound_ctrl:1
	s_nop 1
	v_add_f32_dpp v66, v66, v66 row_mirror row_mask:0xf bank_mask:0xf bound_ctrl:1
	s_nop 1
	v_mov_b32_dpp v67, v66 row_bcast:15 row_mask:0xa bank_mask:0xf
	v_add_f32_e32 v66, v66, v67
	s_nop 0
	v_readlane_b32 s1, v66, 31
	v_readlane_b32 s22, v66, 63
	s_nop 0
	v_mov_b32_e32 v67, s1
	v_mov_b32_e32 v66, s22
	v_cndmask_b32_e64 v66, v66, v67, s[40:41]
	v_fmamk_f32 v66, v66, 0x3c800000, v225
	v_rsq_f32_e32 v84, v66
	v_add_u32_e32 v66, 8, v148
	v_ashrrev_i32_e32 v67, 31, v66
	v_lshlrev_b64 v[66:67], 11, v[66:67]
	v_lshl_add_u64 v[66:67], s[74:75], 0, v[66:67]
	v_mul_f32_e32 v70, v70, v84
	v_lshl_add_u64 v[66:67], v[66:67], 0, s[80:81]
	v_mul_f32_e32 v70, v173, v70
	s_waitcnt lgkmcnt(0)
	v_mul_f32_e32 v68, v68, v70
	v_lshl_add_u64 v[66:67], v[66:67], 0, v[114:115]
	v_bfe_u32 v70, v68, 16, 1
	v_lshl_add_u64 v[82:83], v[66:67], 0, s[6:7]
	v_add_co_u32_e32 v66, vcc, s83, v66
	v_add3_u32 v68, v68, v70, s9
	s_nop 0
	v_addc_co_u32_e32 v67, vcc, 0, v67, vcc
	global_store_short_d16_hi v[66:67], v68, off offset:1024
	v_mul_f32_e32 v66, v86, v84
	v_mul_f32_e32 v66, v176, v66
	v_mul_f32_e32 v66, v69, v66
	v_bfe_u32 v67, v66, 16, 1
	v_add3_u32 v66, v66, v67, s9
	global_store_short_d16_hi v[82:83], v66, off offset:64
	v_mul_f32_e32 v66, v87, v87
	v_fmac_f32_e32 v66, v71, v71
	v_mov_b32_e32 v67, v115
	ds_read2_b32 v[68:69], v205 offset1:32
	v_add_f32_dpp v66, v66, v66 quad_perm:[1,0,3,2] row_mask:0xf bank_mask:0xf bound_ctrl:1
	s_nop 1
	v_add_f32_dpp v66, v66, v66 quad_perm:[2,3,0,1] row_mask:0xf bank_mask:0xf bound_ctrl:1
	s_nop 1
	v_add_f32_dpp v66, v66, v66 row_half_mirror row_mask:0xf bank_mask:0xf bound_ctrl:1
	s_nop 1
	v_add_f32_dpp v66, v66, v66 row_mirror row_mask:0xf bank_mask:0xf bound_ctrl:1
	s_nop 1
	v_mov_b32_dpp v67, v66 row_bcast:15 row_mask:0xa bank_mask:0xf
	v_add_f32_e32 v66, v66, v67
	s_nop 0
	v_readlane_b32 s1, v66, 31
	v_readlane_b32 s22, v66, 63
	s_nop 0
	v_mov_b32_e32 v67, s1
	v_mov_b32_e32 v66, s22
	v_cndmask_b32_e64 v66, v66, v67, s[40:41]
	v_fmamk_f32 v66, v66, 0x3c800000, v225
	v_rsq_f32_e32 v82, v66
	v_add_u32_e32 v66, 9, v148
	v_ashrrev_i32_e32 v67, 31, v66
	v_lshlrev_b64 v[66:67], 11, v[66:67]
	v_mul_f32_e32 v70, v71, v82
	v_lshl_add_u64 v[66:67], s[74:75], 0, v[66:67]
	v_mul_f32_e32 v70, v173, v70
	v_lshl_add_u64 v[66:67], v[66:67], 0, s[80:81]
	s_waitcnt lgkmcnt(0)
	v_mul_f32_e32 v68, v68, v70
	v_bfe_u32 v70, v68, 16, 1
	v_lshl_add_u64 v[66:67], v[66:67], 0, v[114:115]
	v_add3_u32 v68, v68, v70, s9
	v_lshl_add_u64 v[70:71], v[66:67], 0, s[6:7]
	v_add_co_u32_e32 v66, vcc, s83, v66
	s_nop 1
	v_addc_co_u32_e32 v67, vcc, 0, v67, vcc
	global_store_short_d16_hi v[66:67], v68, off offset:1024
	v_mul_f32_e32 v66, v87, v82
	v_mul_f32_e32 v66, v176, v66
	v_mul_f32_e32 v66, v69, v66
	v_bfe_u32 v67, v66, 16, 1
	v_add3_u32 v66, v66, v67, s9
	global_store_short_d16_hi v[70:71], v66, off offset:64
	v_mul_f32_e32 v66, v88, v88
	v_fmac_f32_e32 v66, v72, v72
	v_mov_b32_e32 v67, v115
	ds_read2_b32 v[68:69], v206 offset1:32
	v_add_f32_dpp v66, v66, v66 quad_perm:[1,0,3,2] row_mask:0xf bank_mask:0xf bound_ctrl:1
	s_nop 1
	v_add_f32_dpp v66, v66, v66 quad_perm:[2,3,0,1] row_mask:0xf bank_mask:0xf bound_ctrl:1
	s_nop 1
	v_add_f32_dpp v66, v66, v66 row_half_mirror row_mask:0xf bank_mask:0xf bound_ctrl:1
	s_nop 1
	v_add_f32_dpp v66, v66, v66 row_mirror row_mask:0xf bank_mask:0xf bound_ctrl:1
	s_nop 1
	v_mov_b32_dpp v67, v66 row_bcast:15 row_mask:0xa bank_mask:0xf
	v_add_f32_e32 v66, v66, v67
	s_nop 0
	v_readlane_b32 s1, v66, 31
	v_readlane_b32 s22, v66, 63
	s_nop 0
	v_mov_b32_e32 v67, s1
	v_mov_b32_e32 v66, s22
	v_cndmask_b32_e64 v66, v66, v67, s[40:41]
	v_fmamk_f32 v66, v66, 0x3c800000, v225
	v_rsq_f32_e32 v82, v66
	v_add_u32_e32 v66, 10, v148
	v_ashrrev_i32_e32 v67, 31, v66
	v_lshlrev_b64 v[66:67], 11, v[66:67]
	v_mul_f32_e32 v70, v72, v82
	v_lshl_add_u64 v[66:67], s[74:75], 0, v[66:67]
	v_mul_f32_e32 v70, v173, v70
	v_lshl_add_u64 v[66:67], v[66:67], 0, s[80:81]
	s_waitcnt lgkmcnt(0)
	v_mul_f32_e32 v68, v68, v70
	v_bfe_u32 v70, v68, 16, 1
	v_lshl_add_u64 v[66:67], v[66:67], 0, v[114:115]
	v_add3_u32 v68, v68, v70, s9
	v_lshl_add_u64 v[70:71], v[66:67], 0, s[6:7]
	v_add_co_u32_e32 v66, vcc, s83, v66
	s_nop 1
	v_addc_co_u32_e32 v67, vcc, 0, v67, vcc
	global_store_short_d16_hi v[66:67], v68, off offset:1024
	v_mul_f32_e32 v66, v88, v82
	v_mul_f32_e32 v66, v176, v66
	v_mul_f32_e32 v66, v69, v66
	v_bfe_u32 v67, v66, 16, 1
	v_add3_u32 v66, v66, v67, s9
	global_store_short_d16_hi v[70:71], v66, off offset:64
	v_mul_f32_e32 v66, v89, v89
	v_fmac_f32_e32 v66, v73, v73
	v_mov_b32_e32 v67, v115
	ds_read2_b32 v[68:69], v207 offset1:32
	v_add_f32_dpp v66, v66, v66 quad_perm:[1,0,3,2] row_mask:0xf bank_mask:0xf bound_ctrl:1
	s_nop 1
	v_add_f32_dpp v66, v66, v66 quad_perm:[2,3,0,1] row_mask:0xf bank_mask:0xf bound_ctrl:1
	s_nop 1
	v_add_f32_dpp v66, v66, v66 row_half_mirror row_mask:0xf bank_mask:0xf bound_ctrl:1
	s_nop 1
	v_add_f32_dpp v66, v66, v66 row_mirror row_mask:0xf bank_mask:0xf bound_ctrl:1
	s_nop 1
	v_mov_b32_dpp v67, v66 row_bcast:15 row_mask:0xa bank_mask:0xf
	v_add_f32_e32 v66, v66, v67
	s_nop 0
	v_readlane_b32 s1, v66, 31
	v_readlane_b32 s22, v66, 63
	s_nop 0
	v_mov_b32_e32 v67, s1
	v_mov_b32_e32 v66, s22
	v_cndmask_b32_e64 v66, v66, v67, s[40:41]
	v_fmamk_f32 v66, v66, 0x3c800000, v225
	v_rsq_f32_e32 v72, v66
	v_add_u32_e32 v66, 11, v148
	v_ashrrev_i32_e32 v67, 31, v66
	v_lshlrev_b64 v[66:67], 11, v[66:67]
	v_mul_f32_e32 v70, v73, v72
	v_lshl_add_u64 v[66:67], s[74:75], 0, v[66:67]
	v_mul_f32_e32 v70, v173, v70
	v_lshl_add_u64 v[66:67], v[66:67], 0, s[80:81]
	s_waitcnt lgkmcnt(0)
	v_mul_f32_e32 v68, v68, v70
	v_bfe_u32 v70, v68, 16, 1
	v_lshl_add_u64 v[66:67], v[66:67], 0, v[114:115]
	v_add3_u32 v68, v68, v70, s9
	v_lshl_add_u64 v[70:71], v[66:67], 0, s[6:7]
	v_add_co_u32_e32 v66, vcc, s83, v66
	s_nop 1
	v_addc_co_u32_e32 v67, vcc, 0, v67, vcc
	global_store_short_d16_hi v[66:67], v68, off offset:1024
	v_mul_f32_e32 v66, v89, v72
	v_mul_f32_e32 v66, v176, v66
	v_mul_f32_e32 v66, v69, v66
	v_bfe_u32 v67, v66, 16, 1
	v_add3_u32 v66, v66, v67, s9
	global_store_short_d16_hi v[70:71], v66, off offset:64
	v_mul_f32_e32 v66, v90, v90
	v_fmac_f32_e32 v66, v74, v74
	v_mov_b32_e32 v67, v115
	ds_read2_b32 v[68:69], v208 offset1:32
	v_add_f32_dpp v66, v66, v66 quad_perm:[1,0,3,2] row_mask:0xf bank_mask:0xf bound_ctrl:1
	s_nop 1
	v_add_f32_dpp v66, v66, v66 quad_perm:[2,3,0,1] row_mask:0xf bank_mask:0xf bound_ctrl:1
	s_nop 1
	v_add_f32_dpp v66, v66, v66 row_half_mirror row_mask:0xf bank_mask:0xf bound_ctrl:1
	s_nop 1
	v_add_f32_dpp v66, v66, v66 row_mirror row_mask:0xf bank_mask:0xf bound_ctrl:1
	s_nop 1
	v_mov_b32_dpp v67, v66 row_bcast:15 row_mask:0xa bank_mask:0xf
	v_add_f32_e32 v66, v66, v67
	s_nop 0
	v_readlane_b32 s1, v66, 31
	v_readlane_b32 s22, v66, 63
	s_nop 0
	v_mov_b32_e32 v67, s1
	v_mov_b32_e32 v66, s22
	v_cndmask_b32_e64 v66, v66, v67, s[40:41]
	v_fmamk_f32 v66, v66, 0x3c800000, v225
	v_rsq_f32_e32 v72, v66
	v_add_u32_e32 v66, 16, v148
	v_ashrrev_i32_e32 v67, 31, v66
	v_lshlrev_b64 v[66:67], 11, v[66:67]
	v_mul_f32_e32 v70, v74, v72
	v_lshl_add_u64 v[66:67], s[74:75], 0, v[66:67]
	v_mul_f32_e32 v70, v173, v70
	v_lshl_add_u64 v[66:67], v[66:67], 0, s[80:81]
	s_waitcnt lgkmcnt(0)
	v_mul_f32_e32 v68, v68, v70
	v_bfe_u32 v70, v68, 16, 1
	v_lshl_add_u64 v[66:67], v[66:67], 0, v[114:115]
	v_add3_u32 v68, v68, v70, s9
	v_lshl_add_u64 v[70:71], v[66:67], 0, s[6:7]
	v_add_co_u32_e32 v66, vcc, s83, v66
	s_nop 1
	v_addc_co_u32_e32 v67, vcc, 0, v67, vcc
	global_store_short_d16_hi v[66:67], v68, off offset:1024
	v_mul_f32_e32 v66, v90, v72
	v_mul_f32_e32 v66, v176, v66
	v_mul_f32_e32 v66, v69, v66
	v_bfe_u32 v67, v66, 16, 1
	v_add3_u32 v66, v66, v67, s9
	global_store_short_d16_hi v[70:71], v66, off offset:64
	v_mul_f32_e32 v66, v91, v91
	v_fmac_f32_e32 v66, v75, v75
	v_mov_b32_e32 v67, v115
	ds_read2_b32 v[68:69], v209 offset1:32
	v_add_f32_dpp v66, v66, v66 quad_perm:[1,0,3,2] row_mask:0xf bank_mask:0xf bound_ctrl:1
	s_nop 1
	v_add_f32_dpp v66, v66, v66 quad_perm:[2,3,0,1] row_mask:0xf bank_mask:0xf bound_ctrl:1
	s_nop 1
	v_add_f32_dpp v66, v66, v66 row_half_mirror row_mask:0xf bank_mask:0xf bound_ctrl:1
	s_nop 1
	v_add_f32_dpp v66, v66, v66 row_mirror row_mask:0xf bank_mask:0xf bound_ctrl:1
	s_nop 1
	v_mov_b32_dpp v67, v66 row_bcast:15 row_mask:0xa bank_mask:0xf
	v_add_f32_e32 v66, v66, v67
	s_nop 0
	v_readlane_b32 s1, v66, 31
	v_readlane_b32 s22, v66, 63
	s_nop 0
	v_mov_b32_e32 v67, s1
	v_mov_b32_e32 v66, s22
	v_cndmask_b32_e64 v66, v66, v67, s[40:41]
	v_fmamk_f32 v66, v66, 0x3c800000, v225
	v_rsq_f32_e32 v72, v66
	v_add_u32_e32 v66, 17, v148
	v_ashrrev_i32_e32 v67, 31, v66
	v_lshlrev_b64 v[66:67], 11, v[66:67]
	v_mul_f32_e32 v70, v75, v72
	v_lshl_add_u64 v[66:67], s[74:75], 0, v[66:67]
	v_mul_f32_e32 v70, v173, v70
	v_lshl_add_u64 v[66:67], v[66:67], 0, s[80:81]
	s_waitcnt lgkmcnt(0)
	v_mul_f32_e32 v68, v68, v70
	v_bfe_u32 v70, v68, 16, 1
	v_lshl_add_u64 v[66:67], v[66:67], 0, v[114:115]
	v_add3_u32 v68, v68, v70, s9
	v_lshl_add_u64 v[70:71], v[66:67], 0, s[6:7]
	v_add_co_u32_e32 v66, vcc, s83, v66
	s_nop 1
	v_addc_co_u32_e32 v67, vcc, 0, v67, vcc
	global_store_short_d16_hi v[66:67], v68, off offset:1024
	v_mul_f32_e32 v66, v91, v72
	v_mul_f32_e32 v66, v176, v66
	v_mul_f32_e32 v66, v69, v66
	v_bfe_u32 v67, v66, 16, 1
	v_add3_u32 v66, v66, v67, s9
	global_store_short_d16_hi v[70:71], v66, off offset:64
	v_mul_f32_e32 v66, v92, v92
	v_fmac_f32_e32 v66, v76, v76
	v_mov_b32_e32 v67, v115
	ds_read2_b32 v[68:69], v210 offset1:32
	v_add_f32_dpp v66, v66, v66 quad_perm:[1,0,3,2] row_mask:0xf bank_mask:0xf bound_ctrl:1
	s_nop 1
	v_add_f32_dpp v66, v66, v66 quad_perm:[2,3,0,1] row_mask:0xf bank_mask:0xf bound_ctrl:1
	s_nop 1
	v_add_f32_dpp v66, v66, v66 row_half_mirror row_mask:0xf bank_mask:0xf bound_ctrl:1
	s_nop 1
	v_add_f32_dpp v66, v66, v66 row_mirror row_mask:0xf bank_mask:0xf bound_ctrl:1
	s_nop 1
	v_mov_b32_dpp v67, v66 row_bcast:15 row_mask:0xa bank_mask:0xf
	v_add_f32_e32 v66, v66, v67
	s_nop 0
	v_readlane_b32 s1, v66, 31
	v_readlane_b32 s22, v66, 63
	s_nop 0
	v_mov_b32_e32 v67, s1
	v_mov_b32_e32 v66, s22
	v_cndmask_b32_e64 v66, v66, v67, s[40:41]
	v_fmamk_f32 v66, v66, 0x3c800000, v225
	v_rsq_f32_e32 v72, v66
	v_add_u32_e32 v66, 18, v148
	v_ashrrev_i32_e32 v67, 31, v66
	v_lshlrev_b64 v[66:67], 11, v[66:67]
	v_mul_f32_e32 v70, v76, v72
	v_lshl_add_u64 v[66:67], s[74:75], 0, v[66:67]
	v_mul_f32_e32 v70, v173, v70
	v_lshl_add_u64 v[66:67], v[66:67], 0, s[80:81]
	s_waitcnt lgkmcnt(0)
	v_mul_f32_e32 v68, v68, v70
	v_bfe_u32 v70, v68, 16, 1
	v_lshl_add_u64 v[66:67], v[66:67], 0, v[114:115]
	v_add3_u32 v68, v68, v70, s9
	v_lshl_add_u64 v[70:71], v[66:67], 0, s[6:7]
	v_add_co_u32_e32 v66, vcc, s83, v66
	s_nop 1
	v_addc_co_u32_e32 v67, vcc, 0, v67, vcc
	global_store_short_d16_hi v[66:67], v68, off offset:1024
	v_mul_f32_e32 v66, v92, v72
	v_mul_f32_e32 v66, v176, v66
	v_mul_f32_e32 v66, v69, v66
	v_bfe_u32 v67, v66, 16, 1
	v_add3_u32 v66, v66, v67, s9
	global_store_short_d16_hi v[70:71], v66, off offset:64
	v_mul_f32_e32 v66, v93, v93
	v_fmac_f32_e32 v66, v77, v77
	v_mov_b32_e32 v67, v115
	ds_read2_b32 v[68:69], v211 offset1:32
	v_add_f32_dpp v66, v66, v66 quad_perm:[1,0,3,2] row_mask:0xf bank_mask:0xf bound_ctrl:1
	s_nop 1
	v_add_f32_dpp v66, v66, v66 quad_perm:[2,3,0,1] row_mask:0xf bank_mask:0xf bound_ctrl:1
	s_nop 1
	v_add_f32_dpp v66, v66, v66 row_half_mirror row_mask:0xf bank_mask:0xf bound_ctrl:1
	s_nop 1
	v_add_f32_dpp v66, v66, v66 row_mirror row_mask:0xf bank_mask:0xf bound_ctrl:1
	s_nop 1
	v_mov_b32_dpp v67, v66 row_bcast:15 row_mask:0xa bank_mask:0xf
	v_add_f32_e32 v66, v66, v67
	s_nop 0
	v_readlane_b32 s1, v66, 31
	v_readlane_b32 s22, v66, 63
	s_nop 0
	v_mov_b32_e32 v67, s1
	v_mov_b32_e32 v66, s22
	v_cndmask_b32_e64 v66, v66, v67, s[40:41]
	v_fmamk_f32 v66, v66, 0x3c800000, v225
	v_rsq_f32_e32 v72, v66
	v_add_u32_e32 v66, 19, v148
	v_ashrrev_i32_e32 v67, 31, v66
	v_lshlrev_b64 v[66:67], 11, v[66:67]
	v_mul_f32_e32 v70, v77, v72
	v_lshl_add_u64 v[66:67], s[74:75], 0, v[66:67]
	v_mul_f32_e32 v70, v173, v70
	v_lshl_add_u64 v[66:67], v[66:67], 0, s[80:81]
	s_waitcnt lgkmcnt(0)
	v_mul_f32_e32 v68, v68, v70
	v_bfe_u32 v70, v68, 16, 1
	v_lshl_add_u64 v[66:67], v[66:67], 0, v[114:115]
	v_add3_u32 v68, v68, v70, s9
	v_lshl_add_u64 v[70:71], v[66:67], 0, s[6:7]
	v_add_co_u32_e32 v66, vcc, s83, v66
	s_nop 1
	v_addc_co_u32_e32 v67, vcc, 0, v67, vcc
	global_store_short_d16_hi v[66:67], v68, off offset:1024
	v_mul_f32_e32 v66, v93, v72
	v_mul_f32_e32 v66, v176, v66
	v_mul_f32_e32 v66, v69, v66
	v_bfe_u32 v67, v66, 16, 1
	v_add3_u32 v66, v66, v67, s9
	global_store_short_d16_hi v[70:71], v66, off offset:64
	v_mul_f32_e32 v66, v94, v94
	v_fmac_f32_e32 v66, v78, v78
	v_mov_b32_e32 v67, v115
	ds_read2_b32 v[68:69], v212 offset1:32
	v_add_f32_dpp v66, v66, v66 quad_perm:[1,0,3,2] row_mask:0xf bank_mask:0xf bound_ctrl:1
	s_nop 1
	v_add_f32_dpp v66, v66, v66 quad_perm:[2,3,0,1] row_mask:0xf bank_mask:0xf bound_ctrl:1
	s_nop 1
	v_add_f32_dpp v66, v66, v66 row_half_mirror row_mask:0xf bank_mask:0xf bound_ctrl:1
	s_nop 1
	v_add_f32_dpp v66, v66, v66 row_mirror row_mask:0xf bank_mask:0xf bound_ctrl:1
	s_nop 1
	v_mov_b32_dpp v67, v66 row_bcast:15 row_mask:0xa bank_mask:0xf
	v_add_f32_e32 v66, v66, v67
	s_nop 0
	v_readlane_b32 s1, v66, 31
	v_readlane_b32 s22, v66, 63
	s_nop 0
	v_mov_b32_e32 v67, s1
	v_mov_b32_e32 v66, s22
	v_cndmask_b32_e64 v66, v66, v67, s[40:41]
	v_fmamk_f32 v66, v66, 0x3c800000, v225
	v_rsq_f32_e32 v72, v66
	v_add_u32_e32 v66, 24, v148
	v_ashrrev_i32_e32 v67, 31, v66
	v_lshlrev_b64 v[66:67], 11, v[66:67]
	v_mul_f32_e32 v70, v78, v72
	v_lshl_add_u64 v[66:67], s[74:75], 0, v[66:67]
	v_mul_f32_e32 v70, v173, v70
	v_lshl_add_u64 v[66:67], v[66:67], 0, s[80:81]
	s_waitcnt lgkmcnt(0)
	v_mul_f32_e32 v68, v68, v70
	v_bfe_u32 v70, v68, 16, 1
	v_lshl_add_u64 v[66:67], v[66:67], 0, v[114:115]
	v_add3_u32 v68, v68, v70, s9
	v_lshl_add_u64 v[70:71], v[66:67], 0, s[6:7]
	v_add_co_u32_e32 v66, vcc, s83, v66
	s_nop 1
	v_addc_co_u32_e32 v67, vcc, 0, v67, vcc
	global_store_short_d16_hi v[66:67], v68, off offset:1024
	v_mul_f32_e32 v66, v94, v72
	v_mul_f32_e32 v66, v176, v66
	v_mul_f32_e32 v66, v69, v66
	v_bfe_u32 v67, v66, 16, 1
	v_add3_u32 v66, v66, v67, s9
	global_store_short_d16_hi v[70:71], v66, off offset:64
	v_mul_f32_e32 v66, v95, v95
	v_fmac_f32_e32 v66, v79, v79
	v_mov_b32_e32 v67, v115
	ds_read2_b32 v[68:69], v213 offset1:32
	v_add_f32_dpp v66, v66, v66 quad_perm:[1,0,3,2] row_mask:0xf bank_mask:0xf bound_ctrl:1
	s_nop 1
	v_add_f32_dpp v66, v66, v66 quad_perm:[2,3,0,1] row_mask:0xf bank_mask:0xf bound_ctrl:1
	s_nop 1
	v_add_f32_dpp v66, v66, v66 row_half_mirror row_mask:0xf bank_mask:0xf bound_ctrl:1
	s_nop 1
	v_add_f32_dpp v66, v66, v66 row_mirror row_mask:0xf bank_mask:0xf bound_ctrl:1
	s_nop 1
	v_mov_b32_dpp v67, v66 row_bcast:15 row_mask:0xa bank_mask:0xf
	v_add_f32_e32 v66, v66, v67
	s_nop 0
	v_readlane_b32 s1, v66, 31
	v_readlane_b32 s22, v66, 63
	s_nop 0
	v_mov_b32_e32 v67, s1
	v_mov_b32_e32 v66, s22
	v_cndmask_b32_e64 v66, v66, v67, s[40:41]
	v_fmamk_f32 v66, v66, 0x3c800000, v225
	v_rsq_f32_e32 v72, v66
	v_add_u32_e32 v66, 25, v148
	v_ashrrev_i32_e32 v67, 31, v66
	v_lshlrev_b64 v[66:67], 11, v[66:67]
	v_mul_f32_e32 v70, v79, v72
	v_lshl_add_u64 v[66:67], s[74:75], 0, v[66:67]
	v_mul_f32_e32 v70, v173, v70
	v_lshl_add_u64 v[66:67], v[66:67], 0, s[80:81]
	s_waitcnt lgkmcnt(0)
	v_mul_f32_e32 v68, v68, v70
	v_bfe_u32 v70, v68, 16, 1
	v_lshl_add_u64 v[66:67], v[66:67], 0, v[114:115]
	v_add3_u32 v68, v68, v70, s9
	v_lshl_add_u64 v[70:71], v[66:67], 0, s[6:7]
	v_add_co_u32_e32 v66, vcc, s83, v66
	s_nop 1
	v_addc_co_u32_e32 v67, vcc, 0, v67, vcc
	global_store_short_d16_hi v[66:67], v68, off offset:1024
	v_mul_f32_e32 v66, v95, v72
	v_mul_f32_e32 v66, v176, v66
	v_mul_f32_e32 v66, v69, v66
	v_bfe_u32 v67, v66, 16, 1
	v_add3_u32 v66, v66, v67, s9
	global_store_short_d16_hi v[70:71], v66, off offset:64
	v_mul_f32_e32 v66, v96, v96
	v_fmac_f32_e32 v66, v80, v80
	v_mov_b32_e32 v67, v115
	ds_read2_b32 v[68:69], v214 offset1:32
	v_add_f32_dpp v66, v66, v66 quad_perm:[1,0,3,2] row_mask:0xf bank_mask:0xf bound_ctrl:1
	s_nop 1
	v_add_f32_dpp v66, v66, v66 quad_perm:[2,3,0,1] row_mask:0xf bank_mask:0xf bound_ctrl:1
	s_nop 1
	v_add_f32_dpp v66, v66, v66 row_half_mirror row_mask:0xf bank_mask:0xf bound_ctrl:1
	s_nop 1
	v_add_f32_dpp v66, v66, v66 row_mirror row_mask:0xf bank_mask:0xf bound_ctrl:1
	s_nop 1
	v_mov_b32_dpp v67, v66 row_bcast:15 row_mask:0xa bank_mask:0xf
	v_add_f32_e32 v66, v66, v67
	s_nop 0
	v_readlane_b32 s1, v66, 31
	v_readlane_b32 s22, v66, 63
	s_nop 0
	v_mov_b32_e32 v67, s1
	v_mov_b32_e32 v66, s22
	v_cndmask_b32_e64 v66, v66, v67, s[40:41]
	v_fmamk_f32 v66, v66, 0x3c800000, v225
	v_rsq_f32_e32 v72, v66
	v_add_u32_e32 v66, 26, v148
	v_ashrrev_i32_e32 v67, 31, v66
	v_lshlrev_b64 v[66:67], 11, v[66:67]
	v_mul_f32_e32 v70, v80, v72
	v_lshl_add_u64 v[66:67], s[74:75], 0, v[66:67]
	v_mul_f32_e32 v70, v173, v70
	v_lshl_add_u64 v[66:67], v[66:67], 0, s[80:81]
	s_waitcnt lgkmcnt(0)
	v_mul_f32_e32 v68, v68, v70
	v_bfe_u32 v70, v68, 16, 1
	v_lshl_add_u64 v[66:67], v[66:67], 0, v[114:115]
	v_add3_u32 v68, v68, v70, s9
	v_lshl_add_u64 v[70:71], v[66:67], 0, s[6:7]
	v_add_co_u32_e32 v66, vcc, s83, v66
	s_nop 1
	v_addc_co_u32_e32 v67, vcc, 0, v67, vcc
	global_store_short_d16_hi v[66:67], v68, off offset:1024
	v_mul_f32_e32 v66, v96, v72
	v_mul_f32_e32 v66, v176, v66
	v_mul_f32_e32 v66, v69, v66
	v_bfe_u32 v67, v66, 16, 1
	v_add3_u32 v66, v66, v67, s9
	global_store_short_d16_hi v[70:71], v66, off offset:64
	v_mul_f32_e32 v66, v97, v97
	v_fmac_f32_e32 v66, v81, v81
	v_mov_b32_e32 v67, v115
	ds_read2_b32 v[68:69], v215 offset1:32
	v_add_f32_dpp v66, v66, v66 quad_perm:[1,0,3,2] row_mask:0xf bank_mask:0xf bound_ctrl:1
	s_nop 1
	v_add_f32_dpp v66, v66, v66 quad_perm:[2,3,0,1] row_mask:0xf bank_mask:0xf bound_ctrl:1
	s_nop 1
	v_add_f32_dpp v66, v66, v66 row_half_mirror row_mask:0xf bank_mask:0xf bound_ctrl:1
	s_nop 1
	v_add_f32_dpp v66, v66, v66 row_mirror row_mask:0xf bank_mask:0xf bound_ctrl:1
	s_nop 1
	v_mov_b32_dpp v67, v66 row_bcast:15 row_mask:0xa bank_mask:0xf
	v_add_f32_e32 v66, v66, v67
	s_nop 0
	v_readlane_b32 s1, v66, 31
	v_readlane_b32 s22, v66, 63
	s_nop 0
	v_mov_b32_e32 v67, s1
	v_mov_b32_e32 v66, s22
	v_cndmask_b32_e64 v66, v66, v67, s[40:41]
	v_fmamk_f32 v66, v66, 0x3c800000, v225
	v_rsq_f32_e32 v72, v66
	v_add_u32_e32 v66, 27, v148
	v_ashrrev_i32_e32 v67, 31, v66
	v_lshlrev_b64 v[66:67], 11, v[66:67]
	v_mul_f32_e32 v70, v81, v72
	v_lshl_add_u64 v[66:67], s[74:75], 0, v[66:67]
	v_mul_f32_e32 v70, v173, v70
	v_lshl_add_u64 v[66:67], v[66:67], 0, s[80:81]
	s_waitcnt lgkmcnt(0)
	v_mul_f32_e32 v68, v68, v70
	v_bfe_u32 v70, v68, 16, 1
	v_lshl_add_u64 v[66:67], v[66:67], 0, v[114:115]
	v_add3_u32 v68, v68, v70, s9
	v_lshl_add_u64 v[70:71], v[66:67], 0, s[6:7]
	v_add_co_u32_e32 v66, vcc, s83, v66
	s_nop 1
	v_addc_co_u32_e32 v67, vcc, 0, v67, vcc
	global_store_short_d16_hi v[66:67], v68, off offset:1024
	v_mul_f32_e32 v66, v97, v72
	v_mul_f32_e32 v66, v176, v66
	v_mul_f32_e32 v66, v69, v66
	v_bfe_u32 v67, v66, 16, 1
	v_add3_u32 v66, v66, v67, s9
	global_store_short_d16_hi v[70:71], v66, off offset:64
	s_cbranch_scc0 .LBB0_998
	s_branch .LBB0_913

.LBB0_1213:
	s_or_b64 exec, exec, s[22:23]
	v_lshlrev_b32_e32 v80, 16, v124
	v_and_b32_e32 v10, 0xffff0000, v124
	v_mul_f32_e32 v10, v10, v10
	v_fmac_f32_e32 v10, v80, v80
	v_lshlrev_b32_e32 v80, 16, v125
	v_and_b32_e32 v11, 0xffff0000, v125
	v_mul_f32_e32 v11, v11, v11
	v_fmac_f32_e32 v11, v80, v80
	v_lshlrev_b32_e32 v80, 16, v126
	v_and_b32_e32 v12, 0xffff0000, v126
	v_mul_f32_e32 v12, v12, v12
	v_fmac_f32_e32 v12, v80, v80
	v_lshlrev_b32_e32 v80, 16, v127
	v_and_b32_e32 v13, 0xffff0000, v127
	v_add_f32_e32 v10, v110, v10
	v_mul_f32_e32 v13, v13, v13
	v_add_f32_e32 v10, v11, v10
	v_fmac_f32_e32 v13, v80, v80
	v_add_f32_e32 v10, v12, v10
	v_and_b32_e32 v12, 0xffff0000, v128
	v_add_f32_e32 v10, v13, v10
	v_lshlrev_b32_e32 v11, 16, v128
	v_mul_f32_e32 v12, v12, v12
	v_and_b32_e32 v13, 0xffff0000, v129
	v_fmac_f32_e32 v12, v11, v11
	v_lshlrev_b32_e32 v11, 16, v129
	v_mul_f32_e32 v13, v13, v13
	v_and_b32_e32 v14, 0xffff0000, v130
	v_fmac_f32_e32 v13, v11, v11
	v_lshlrev_b32_e32 v11, 16, v130
	v_mul_f32_e32 v14, v14, v14
	v_and_b32_e32 v15, 0xffff0000, v131
	v_add_f32_e32 v10, v10, v12
	v_fmac_f32_e32 v14, v11, v11
	v_lshlrev_b32_e32 v11, 16, v131
	v_mul_f32_e32 v15, v15, v15
	v_add_f32_e32 v10, v13, v10
	v_and_b32_e32 v12, 0xffff0000, v132
	v_fmac_f32_e32 v15, v11, v11
	v_add_f32_e32 v10, v14, v10
	v_lshlrev_b32_e32 v11, 16, v132
	v_mul_f32_e32 v12, v12, v12
	v_and_b32_e32 v13, 0xffff0000, v133
	v_add_f32_e32 v10, v15, v10
	v_fmac_f32_e32 v12, v11, v11
	v_lshlrev_b32_e32 v11, 16, v133
	v_mul_f32_e32 v13, v13, v13
	v_and_b32_e32 v14, 0xffff0000, v134
	v_fmac_f32_e32 v13, v11, v11
	v_lshlrev_b32_e32 v11, 16, v134
	v_mul_f32_e32 v14, v14, v14
	v_and_b32_e32 v15, 0xffff0000, v135
	v_add_f32_e32 v10, v10, v12
	v_fmac_f32_e32 v14, v11, v11
	v_lshlrev_b32_e32 v11, 16, v135
	v_mul_f32_e32 v15, v15, v15
	v_add_f32_e32 v10, v13, v10
	v_and_b32_e32 v12, 0xffff0000, v136
	v_fmac_f32_e32 v15, v11, v11
	v_add_f32_e32 v10, v14, v10
	v_lshlrev_b32_e32 v11, 16, v136
	v_mul_f32_e32 v12, v12, v12
	v_and_b32_e32 v13, 0xffff0000, v137
	v_add_f32_e32 v10, v15, v10
	v_fmac_f32_e32 v12, v11, v11
	v_lshlrev_b32_e32 v11, 16, v137
	v_mul_f32_e32 v13, v13, v13
	v_and_b32_e32 v14, 0xffff0000, v138
	v_fmac_f32_e32 v13, v11, v11
	v_lshlrev_b32_e32 v11, 16, v138
	v_mul_f32_e32 v14, v14, v14
	v_and_b32_e32 v15, 0xffff0000, v139
	v_add_f32_e32 v10, v10, v12
	v_fmac_f32_e32 v14, v11, v11
	v_lshlrev_b32_e32 v11, 16, v139
	v_mul_f32_e32 v15, v15, v15
	v_add_f32_e32 v10, v13, v10
	v_and_b32_e32 v12, 0xffff0000, v140
	v_fmac_f32_e32 v15, v11, v11
	v_add_f32_e32 v10, v14, v10
	v_lshlrev_b32_e32 v11, 16, v140
	v_mul_f32_e32 v12, v12, v12
	v_and_b32_e32 v13, 0xffff0000, v141
	v_add_f32_e32 v10, v15, v10
	v_fmac_f32_e32 v12, v11, v11
	v_lshlrev_b32_e32 v11, 16, v141
	v_mul_f32_e32 v13, v13, v13
	v_and_b32_e32 v14, 0xffff0000, v142
	v_fmac_f32_e32 v13, v11, v11
	v_lshlrev_b32_e32 v11, 16, v142
	v_mul_f32_e32 v14, v14, v14
	v_and_b32_e32 v15, 0xffff0000, v143
	v_add_f32_e32 v10, v10, v12
	v_fmac_f32_e32 v14, v11, v11
	v_lshlrev_b32_e32 v11, 16, v143
	v_mul_f32_e32 v15, v15, v15
	v_add_f32_e32 v10, v13, v10
	v_and_b32_e32 v12, 0xffff0000, v144
	v_fmac_f32_e32 v15, v11, v11
	v_add_f32_e32 v10, v14, v10
	v_lshlrev_b32_e32 v11, 16, v144
	v_mul_f32_e32 v12, v12, v12
	v_and_b32_e32 v13, 0xffff0000, v145
	v_add_f32_e32 v10, v15, v10
	v_fmac_f32_e32 v12, v11, v11
	v_lshlrev_b32_e32 v11, 16, v145
	v_mul_f32_e32 v13, v13, v13
	v_and_b32_e32 v14, 0xffff0000, v146
	v_fmac_f32_e32 v13, v11, v11
	v_lshlrev_b32_e32 v11, 16, v146
	v_mul_f32_e32 v14, v14, v14
	v_and_b32_e32 v15, 0xffff0000, v147
	v_add_f32_e32 v10, v10, v12
	v_fmac_f32_e32 v14, v11, v11
	v_lshlrev_b32_e32 v11, 16, v147
	v_mul_f32_e32 v15, v15, v15
	v_add_f32_e32 v10, v13, v10
	v_and_b32_e32 v12, 0xffff0000, v148
	v_fmac_f32_e32 v15, v11, v11
	v_add_f32_e32 v10, v14, v10
	v_lshlrev_b32_e32 v11, 16, v148
	v_mul_f32_e32 v12, v12, v12
	v_and_b32_e32 v13, 0xffff0000, v149
	v_add_f32_e32 v10, v15, v10
	v_fmac_f32_e32 v12, v11, v11
	v_lshlrev_b32_e32 v11, 16, v149
	v_mul_f32_e32 v13, v13, v13
	v_and_b32_e32 v14, 0xffff0000, v150
	v_fmac_f32_e32 v13, v11, v11
	v_lshlrev_b32_e32 v11, 16, v150
	v_mul_f32_e32 v14, v14, v14
	v_and_b32_e32 v15, 0xffff0000, v151
	v_add_f32_e32 v10, v10, v12
	v_fmac_f32_e32 v14, v11, v11
	v_lshlrev_b32_e32 v11, 16, v151
	v_mul_f32_e32 v15, v15, v15
	v_add_f32_e32 v10, v13, v10
	v_fmac_f32_e32 v15, v11, v11
	v_add_f32_e32 v10, v14, v10
	v_and_b32_e32 v11, 0xffff0000, v152
	v_add_f32_e32 v18, v15, v10
	v_lshlrev_b32_e32 v10, 16, v152
	v_mul_f32_e32 v19, v11, v11
	v_and_b32_e32 v11, 0xffff0000, v153
	v_fmac_f32_e32 v19, v10, v10
	v_lshlrev_b32_e32 v10, 16, v153
	v_mul_f32_e32 v20, v11, v11
	v_and_b32_e32 v11, 0xffff0000, v154
	v_fmac_f32_e32 v20, v10, v10
	v_lshlrev_b32_e32 v10, 16, v154
	v_mul_f32_e32 v21, v11, v11
	v_fmac_f32_e32 v21, v10, v10
	s_waitcnt lgkmcnt(1)
	v_mfma_f32_16x16x32_bf16 v[10:13], v[152:155], v[50:53], v[42:45]
	v_and_b32_e32 v15, 0xffff0000, v155
	v_lshlrev_b32_e32 v14, 16, v155
	v_mul_f32_e32 v22, v15, v15
	v_fmac_f32_e32 v22, v14, v14
	s_waitcnt lgkmcnt(0)
	v_mfma_f32_16x16x32_bf16 v[14:17], v[152:155], v[46:49], v[10:13]
	s_add_u32 s0, s0, 0x200
	s_addc_u32 s1, s1, 0
	s_cmpk_eq_i32 s0, 0x800
	v_add_f32_e32 v10, v18, v19
	v_add_f32_e32 v10, v20, v10
	v_add_f32_e32 v10, v21, v10
	v_add_f32_e32 v110, v22, v10
	v_add_u32_e32 v67, 32, v67
	s_cbranch_scc1 .LBB0_1230
.LBB0_1214:
	v_lshl_add_u64 v[80:81], v[78:79], 0, s[0:1]
	s_mov_b64 s[22:23], 0x29151000
	v_lshl_add_u64 v[120:121], v[80:81], 0, s[22:23]
	global_load_dwordx4 v[124:127], v[120:121], off offset:1280
	global_load_dwordx4 v[128:131], v[120:121], off offset:1344
	global_load_dwordx4 v[132:135], v[120:121], off offset:1408
	global_load_dwordx4 v[136:139], v[120:121], off offset:1472
	global_load_dwordx4 v[140:143], v[120:121], off offset:1536
	global_load_dwordx4 v[144:147], v[120:121], off offset:1600
	global_load_dwordx4 v[148:151], v[120:121], off offset:1664
	global_load_dwordx4 v[152:155], v[120:121], off offset:1728
	s_mov_b32 s22, 0x29151000
	v_add_co_u32_e32 v10, vcc, s22, v80
	v_subrev_u32_e32 v18, 28, v67
	s_nop 0
	v_addc_co_u32_e32 v11, vcc, 0, v81, vcc
	v_xor_b32_e32 v18, v18, v1
	v_lshlrev_b32_e32 v18, 4, v18
	s_add_i32 s24, 0, 0x12000
	v_add_u32_e32 v26, 0, v18
	v_add_u32_e32 v27, s24, v18
	v_lshlrev_b32_e32 v111, 1, v82
	v_add_u32_e32 v28, v27, v111
	v_add_u32_e32 v29, v26, v111
	ds_read_b128 v[18:21], v28
	ds_read_b128 v[22:25], v29
	s_waitcnt vmcnt(7) lgkmcnt(0)
	v_mfma_f32_16x16x32_bf16 v[6:9], v[124:127], v[22:25], v[6:9]
	v_mfma_f32_16x16x32_bf16 v[6:9], v[124:127], v[18:21], v[6:9]
	ds_read_b128 v[18:21], v28 offset:32768
	ds_read_b128 v[22:25], v29 offset:32768
	s_waitcnt lgkmcnt(0)
	v_mfma_f32_16x16x32_bf16 v[2:5], v[124:127], v[22:25], v[2:5]
	v_mov_b32_e32 v22, 0
	v_mov_b32_e32 v23, 0
	v_mov_b32_e32 v24, 0
	v_mfma_f32_16x16x32_bf16 v[18:21], v[124:127], v[18:21], v[2:5]
	v_mov_b32_e32 v25, 0
	s_nop 2
	v_mov_b32_e32 v2, 0
	v_mov_b32_e32 v3, 0
	v_mov_b32_e32 v4, 0
	v_mov_b32_e32 v5, 0
	s_and_saveexec_b64 s[22:23], s[44:45]
	s_cbranch_execz .LBB0_1216
	v_add_u32_e32 v2, v27, v109
	v_add_u32_e32 v3, v26, v109
	ds_read_b128 v[22:25], v3
	ds_read_b128 v[2:5], v2
.LBB0_1216:
	s_or_b64 exec, exec, s[22:23]
	s_waitcnt lgkmcnt(1)
	v_mfma_f32_16x16x32_bf16 v[14:17], v[124:127], v[22:25], v[14:17]
	v_subrev_u32_e32 v22, 24, v67
	v_xor_b32_e32 v22, v22, v1
	v_lshlrev_b32_e32 v22, 4, v22
	s_waitcnt lgkmcnt(0)
	v_mfma_f32_16x16x32_bf16 v[2:5], v[124:127], v[2:5], v[14:17]
	v_add_u32_e32 v38, 0, v22
	v_add_u32_e32 v39, s24, v22
	v_add_u32_e32 v30, v39, v111
	v_add_co_u32_e32 v14, vcc, 0x29151000, v80
	v_add_u32_e32 v31, v38, v111
	s_nop 0
	v_addc_co_u32_e32 v15, vcc, 0, v81, vcc
	ds_read_b128 v[22:25], v30
	ds_read_b128 v[26:29], v31
	v_mov_b32_e32 v32, 0
	v_mov_b32_e32 v33, 0
	v_mov_b32_e32 v34, 0
	v_mov_b32_e32 v35, 0
	v_mov_b32_e32 v36, 0
	v_mov_b32_e32 v37, 0
	s_waitcnt vmcnt(6) lgkmcnt(0)
	v_mfma_f32_16x16x32_bf16 v[6:9], v[128:131], v[26:29], v[6:9]
	v_mfma_f32_16x16x32_bf16 v[22:25], v[128:131], v[22:25], v[6:9]
	s_nop 6
	ds_read_b128 v[6:9], v30 offset:32768
	ds_read_b128 v[26:29], v31 offset:32768
	v_mov_b32_e32 v30, 0
	v_mov_b32_e32 v31, 0
	s_waitcnt lgkmcnt(0)
	v_mfma_f32_16x16x32_bf16 v[18:21], v[128:131], v[26:29], v[18:21]
	v_mfma_f32_16x16x32_bf16 v[26:29], v[128:131], v[6:9], v[18:21]
	v_mov_b32_e32 v6, 0
	s_and_saveexec_b64 s[22:23], s[44:45]
	s_cbranch_execz .LBB0_1218
	v_add_u32_e32 v8, v38, v109
	v_add_u32_e32 v7, v39, v109
	ds_read_b128 v[34:37], v8
	ds_read_b128 v[30:33], v7
.LBB0_1218:
	s_or_b64 exec, exec, s[22:23]
	v_add_co_u32_e32 v8, vcc, 0x29151000, v80
	v_subrev_u32_e32 v7, 20, v67
	s_nop 0
	v_addc_co_u32_e32 v9, vcc, 0, v81, vcc
	s_waitcnt lgkmcnt(1)
	v_mfma_f32_16x16x32_bf16 v[2:5], v[128:131], v[34:37], v[2:5]
	v_xor_b32_e32 v7, v7, v1
	v_lshlrev_b32_e32 v7, 4, v7
	v_add_u32_e32 v34, 0, v7
	v_add_u32_e32 v8, v34, v111
	s_waitcnt lgkmcnt(0)
	v_mfma_f32_16x16x32_bf16 v[2:5], v[128:131], v[30:33], v[2:5]
	ds_read_b128 v[30:33], v8
	ds_read_b128 v[36:39], v8 offset:32768
	v_add_u32_e32 v35, s24, v7
	v_add_u32_e32 v7, v35, v111
	v_mov_b32_e32 v8, 0
	v_mov_b32_e32 v9, 0
	s_waitcnt vmcnt(5) lgkmcnt(1)
	v_mfma_f32_16x16x32_bf16 v[22:25], v[132:135], v[30:33], v[22:25]
	s_waitcnt lgkmcnt(0)
	v_mfma_f32_16x16x32_bf16 v[26:29], v[132:135], v[36:39], v[26:29]
	ds_read_b128 v[30:33], v7
	ds_read_b128 v[36:39], v7 offset:32768
	v_mov_b32_e32 v7, 0
	s_waitcnt lgkmcnt(1)
	v_mfma_f32_16x16x32_bf16 v[30:33], v[132:135], v[30:33], v[22:25]
	s_nop 2
	v_mov_b32_e32 v22, 0
	s_waitcnt lgkmcnt(0)
	v_mfma_f32_16x16x32_bf16 v[26:29], v[132:135], v[36:39], v[26:29]
	v_mov_b32_e32 v23, 0
	v_mov_b32_e32 v24, 0
	v_mov_b32_e32 v25, 0
	s_and_saveexec_b64 s[22:23], s[44:45]
	s_cbranch_execz .LBB0_1220
	v_add_u32_e32 v6, v35, v109
	v_add_u32_e32 v7, v34, v109
	ds_read_b128 v[22:25], v7
	ds_read_b128 v[6:9], v6
.LBB0_1220:
	s_or_b64 exec, exec, s[22:23]
	s_waitcnt lgkmcnt(1)
	v_mfma_f32_16x16x32_bf16 v[2:5], v[132:135], v[22:25], v[2:5]
	v_mov_b32_e32 v42, 0
	v_mov_b32_e32 v43, 0
	v_mov_b32_e32 v44, 0
	s_waitcnt lgkmcnt(0)
	v_mfma_f32_16x16x32_bf16 v[2:5], v[132:135], v[6:9], v[2:5]
	v_add_co_u32_e32 v6, vcc, 0x29151000, v80
	v_mov_b32_e32 v45, 0
	s_nop 0
	v_addc_co_u32_e32 v7, vcc, 0, v81, vcc
	v_add_u32_e32 v6, -16, v67
	v_xor_b32_e32 v6, v6, v1
	v_lshlrev_b32_e32 v6, 4, v6
	v_add_u32_e32 v7, 0, v6
	v_add_u32_e32 v8, s24, v6
	v_add_u32_e32 v6, v8, v111
	v_add_u32_e32 v9, v7, v111
	ds_read_b128 v[34:37], v6
	ds_read_b128 v[38:41], v9
	s_waitcnt vmcnt(4) lgkmcnt(0)
	v_mfma_f32_16x16x32_bf16 v[30:33], v[136:139], v[38:41], v[30:33]
	v_mfma_f32_16x16x32_bf16 v[30:33], v[136:139], v[34:37], v[30:33]
	ds_read_b128 v[34:37], v6 offset:32768
	ds_read_b128 v[38:41], v9 offset:32768
	v_mov_b32_e32 v6, 0
	s_waitcnt lgkmcnt(0)
	v_mfma_f32_16x16x32_bf16 v[26:29], v[136:139], v[38:41], v[26:29]
	v_mov_b32_e32 v38, 0
	v_mov_b32_e32 v39, 0
	v_mov_b32_e32 v40, 0
	v_mfma_f32_16x16x32_bf16 v[34:37], v[136:139], v[34:37], v[26:29]
	v_mov_b32_e32 v41, 0
	s_and_saveexec_b64 s[22:23], s[44:45]
	s_cbranch_execz .LBB0_1222
	v_add_u32_e32 v7, v7, v109
	v_add_u32_e32 v8, v8, v109
	ds_read_b128 v[42:45], v7
	ds_read_b128 v[38:41], v8
.LBB0_1222:
	s_or_b64 exec, exec, s[22:23]
	v_add_co_u32_e32 v8, vcc, 0x29151000, v80
	v_add_u32_e32 v7, -12, v67
	s_nop 0
	v_addc_co_u32_e32 v9, vcc, 0, v81, vcc
	s_waitcnt lgkmcnt(1)
	v_mfma_f32_16x16x32_bf16 v[2:5], v[136:139], v[42:45], v[2:5]
	v_xor_b32_e32 v7, v7, v1
	v_lshlrev_b32_e32 v7, 4, v7
	v_add_u32_e32 v42, 0, v7
	v_add_u32_e32 v8, v42, v111
	s_waitcnt lgkmcnt(0)
	v_mfma_f32_16x16x32_bf16 v[2:5], v[136:139], v[38:41], v[2:5]
	ds_read_b128 v[38:41], v8
	ds_read_b128 v[44:47], v8 offset:32768
	v_add_u32_e32 v43, s24, v7
	v_add_u32_e32 v7, v43, v111
	v_mov_b32_e32 v8, 0
	v_mov_b32_e32 v9, 0
	s_waitcnt vmcnt(3) lgkmcnt(1)
	v_mfma_f32_16x16x32_bf16 v[30:33], v[140:143], v[38:41], v[30:33]
	s_waitcnt lgkmcnt(0)
	v_mfma_f32_16x16x32_bf16 v[34:37], v[140:143], v[44:47], v[34:37]
	ds_read_b128 v[38:41], v7
	ds_read_b128 v[44:47], v7 offset:32768
	v_mov_b32_e32 v7, 0
	s_waitcnt lgkmcnt(1)
	v_mfma_f32_16x16x32_bf16 v[38:41], v[140:143], v[38:41], v[30:33]
	s_nop 2
	v_mov_b32_e32 v30, 0
	s_waitcnt lgkmcnt(0)
	v_mfma_f32_16x16x32_bf16 v[34:37], v[140:143], v[44:47], v[34:37]
	v_mov_b32_e32 v31, 0
	v_mov_b32_e32 v32, 0
	v_mov_b32_e32 v33, 0
	s_and_saveexec_b64 s[22:23], s[44:45]
	s_cbranch_execz .LBB0_1224
	v_add_u32_e32 v6, v43, v109
	v_add_u32_e32 v7, v42, v109
	ds_read_b128 v[30:33], v7
	ds_read_b128 v[6:9], v6
.LBB0_1224:
	s_or_b64 exec, exec, s[22:23]
	s_waitcnt lgkmcnt(1)
	v_mfma_f32_16x16x32_bf16 v[2:5], v[140:143], v[30:33], v[2:5]
	v_mov_b32_e32 v50, 0
	v_mov_b32_e32 v51, 0
	v_mov_b32_e32 v52, 0
	s_waitcnt lgkmcnt(0)
	v_mfma_f32_16x16x32_bf16 v[4:7], v[140:143], v[6:9], v[2:5]
	v_mov_b32_e32 v53, 0
	s_nop 1
	v_add_co_u32_e32 v2, vcc, 0x29151000, v80
	s_nop 1
	v_addc_co_u32_e32 v3, vcc, 0, v81, vcc
	v_add_u32_e32 v2, -8, v67
	v_xor_b32_e32 v2, v2, v1
	v_lshlrev_b32_e32 v2, 4, v2
	v_add_u32_e32 v3, 0, v2
	v_add_u32_e32 v8, s24, v2
	v_add_u32_e32 v2, v8, v111
	v_add_u32_e32 v9, v3, v111
	ds_read_b128 v[42:45], v2
	ds_read_b128 v[46:49], v9
	s_waitcnt vmcnt(2) lgkmcnt(0)
	v_mfma_f32_16x16x32_bf16 v[38:41], v[144:147], v[46:49], v[38:41]
	v_mfma_f32_16x16x32_bf16 v[38:41], v[144:147], v[42:45], v[38:41]
	ds_read_b128 v[42:45], v2 offset:32768
	ds_read_b128 v[46:49], v9 offset:32768
	v_mov_b32_e32 v2, 0
	s_waitcnt lgkmcnt(0)
	v_mfma_f32_16x16x32_bf16 v[34:37], v[144:147], v[46:49], v[34:37]
	v_mov_b32_e32 v46, 0
	v_mov_b32_e32 v47, 0
	v_mov_b32_e32 v48, 0
	v_mfma_f32_16x16x32_bf16 v[42:45], v[144:147], v[42:45], v[34:37]
	v_mov_b32_e32 v49, 0
	s_and_saveexec_b64 s[22:23], s[44:45]
	s_cbranch_execz .LBB0_1226
	v_add_u32_e32 v3, v3, v109
	v_add_u32_e32 v8, v8, v109
	ds_read_b128 v[50:53], v3
	ds_read_b128 v[46:49], v8
.LBB0_1226:
	s_or_b64 exec, exec, s[22:23]
	v_add_co_u32_e32 v8, vcc, 0x29151000, v80
	v_add_u32_e32 v3, -4, v67
	s_nop 0
	v_addc_co_u32_e32 v9, vcc, 0, v81, vcc
	s_waitcnt lgkmcnt(1)
	v_mfma_f32_16x16x32_bf16 v[4:7], v[144:147], v[50:53], v[4:7]
	v_xor_b32_e32 v3, v3, v1
	v_lshlrev_b32_e32 v3, 4, v3
	v_add_u32_e32 v112, 0, v3
	v_add_u32_e32 v8, v112, v111
	s_waitcnt lgkmcnt(0)
	v_mfma_f32_16x16x32_bf16 v[50:53], v[144:147], v[46:49], v[4:7]
	s_nop 2
	ds_read_b128 v[4:7], v8
	ds_read_b128 v[46:49], v8 offset:32768
	s_waitcnt vmcnt(1) lgkmcnt(1)
	v_mfma_f32_16x16x32_bf16 v[4:7], v[148:151], v[4:7], v[38:41]
	s_nop 2
	v_add_u32_e32 v38, s24, v3
	v_add_u32_e32 v3, v38, v111
	s_waitcnt lgkmcnt(0)
	v_mfma_f32_16x16x32_bf16 v[40:43], v[148:151], v[46:49], v[42:45]
	s_nop 2
	ds_read_b128 v[44:47], v3
	ds_read_b128 v[116:119], v3 offset:32768
	v_mov_b32_e32 v3, 0
	s_waitcnt lgkmcnt(1)
	v_mfma_f32_16x16x32_bf16 v[46:49], v[148:151], v[44:47], v[4:7]
	v_mov_b32_e32 v44, 0
	v_mov_b32_e32 v45, 0
	s_nop 0
	v_mov_b32_e32 v4, 0
	s_waitcnt lgkmcnt(0)
	v_mfma_f32_16x16x32_bf16 v[6:9], v[148:151], v[116:119], v[40:43]
	v_mov_b32_e32 v5, 0
	s_nop 1
	v_mov_b32_e32 v42, 0
	v_mov_b32_e32 v43, 0
	s_and_saveexec_b64 s[22:23], s[44:45]
	s_cbranch_execz .LBB0_1228
	v_add_u32_e32 v2, v38, v109
	v_add_u32_e32 v3, v112, v109
	ds_read_b128 v[42:45], v3
	ds_read_b128 v[2:5], v2
.LBB0_1228:
	s_or_b64 exec, exec, s[22:23]
	v_add_co_u32_e32 v38, vcc, 0x29151000, v80
	s_waitcnt lgkmcnt(1)
	v_mfma_f32_16x16x32_bf16 v[42:45], v[148:151], v[42:45], v[50:53]
	v_addc_co_u32_e32 v39, vcc, 0, v81, vcc
	s_nop 0
	v_xor_b32_e32 v50, v67, v1
	v_lshlrev_b32_e32 v81, 4, v50
	v_add_u32_e32 v80, 0, v81
	v_add_u32_e32 v50, v80, v111
	s_waitcnt lgkmcnt(0)
	v_mfma_f32_16x16x32_bf16 v[42:45], v[148:151], v[2:5], v[42:45]
	ds_read_b128 v[2:5], v50
	ds_read_b128 v[50:53], v50 offset:32768
	v_add_u32_e32 v81, s24, v81
	s_waitcnt vmcnt(0) lgkmcnt(1)
	v_mfma_f32_16x16x32_bf16 v[2:5], v[152:155], v[2:5], v[46:49]
	s_nop 2
	v_add_u32_e32 v47, v81, v111
	ds_read_b128 v[116:119], v47 offset:32768
	v_mov_b32_e32 v46, 0
	s_waitcnt lgkmcnt(1)
	v_mfma_f32_16x16x32_bf16 v[50:53], v[152:155], v[50:53], v[6:9]
	v_mov_b32_e32 v48, 0
	v_mov_b32_e32 v49, 0
	s_nop 0
	ds_read_b128 v[6:9], v47
	s_waitcnt lgkmcnt(0)
	v_mfma_f32_16x16x32_bf16 v[6:9], v[152:155], v[6:9], v[2:5]
	v_mov_b32_e32 v47, 0
	v_mfma_f32_16x16x32_bf16 v[2:5], v[152:155], v[116:119], v[50:53]
	s_nop 2
	v_mov_b32_e32 v50, 0
	v_mov_b32_e32 v51, 0
	v_mov_b32_e32 v52, 0
	v_mov_b32_e32 v53, 0
	s_and_saveexec_b64 s[22:23], s[44:45]
	s_cbranch_execz .LBB0_1213
	v_add_u32_e32 v46, v81, v109
	v_add_u32_e32 v47, v80, v109
	ds_read_b128 v[50:53], v47
	ds_read_b128 v[46:49], v46
	s_branch .LBB0_1213
